# speedup vs baseline: 1.0132x; 1.0132x over previous
.LBB1_2:
	s_or_b64 exec, exec, s[4:5]
	v_add_f32_e32 v1, v7, v216
	v_max_f32_e32 v8, 0, v1
	v_sub_f32_e32 v9, v1, v8
	v_fma_f32 v1, v1, s7, -v8
	v_mul_f32_e32 v1, 0x3fb8aa3b, v1
	v_mul_f32_e32 v8, 0xbfb8aa3b, v8
	v_exp_f32_e32 v1, v1
	v_exp_f32_e32 v8, v8
	v_add_f32_e32 v6, v7, v217
	v_max_f32_e32 v7, 0, v6
	v_mul_f32_e32 v10, 0x46000000, v1
	v_fma_mixlo_f16 v15, v1, s6, 0
	v_mul_f32_e32 v1, 0x46000000, v8
	v_sub_f32_e32 v8, v6, v7
	v_fma_f32 v6, v6, s7, -v7
	v_mul_f32_e32 v9, 0x3fb8aa3b, v9
	v_mul_f32_e32 v6, 0x3fb8aa3b, v6
	v_mul_f32_e32 v7, 0xbfb8aa3b, v7
	v_exp_f32_e32 v9, v9
	v_exp_f32_e32 v6, v6
	v_exp_f32_e32 v7, v7
	v_mul_f32_e32 v8, 0x3fb8aa3b, v8
	v_lshrrev_b32_e32 v5, 1, v5
	v_exp_f32_e32 v16, v8
	v_and_b32_e32 v5, 16, v5
	v_or_b32_e32 v142, 0x1b000, v5
	v_cvt_f16_f32_e32 v14, v9
	v_cvt_pk_f16_f32 v136, v9, v9
	v_cvt_pk_f16_f32 v137, v10, v10
	v_mul_f32_e32 v18, 0x46000000, v6
	v_fma_mixlo_f16 v22, v6, s6, 0
	v_mul_f32_e32 v19, 0x46000000, v7
	s_waitcnt lgkmcnt(0)
	s_barrier
	v_or_b32_e32 v143, 0x1b800, v5
	ds_read_b128 v[6:9], v142
	ds_read_b128 v[10:13], v143
	v_cvt_f16_f32_e32 v17, v16
	s_load_dwordx16 s[4:19], s[0:1], 0x0
	v_cvt_pk_f16_f32 v140, v16, v16
	v_cvt_pk_f16_f32 v139, v18, v18
	s_waitcnt lgkmcnt(0)
	v_pk_mul_f16 v16, v6, v14 op_sel_hi:[1,0]
	v_pk_mul_f16 v18, v10, v15 op_sel_hi:[1,0]
	v_cvt_pk_f16_f32 v1, v1, v1
	v_pk_max_f16 v16, v16, v18
	v_pk_mul_f16 v6, v6, v17 op_sel_hi:[1,0]
	v_pk_mul_f16 v10, v10, v22 op_sel_hi:[1,0]
	s_mov_b32 s33, 0x7060100
	v_pk_max_f16 v6, v6, v10
	v_cndmask_b32_e64 v10, v1, v16, s[4:5]
	v_cndmask_b32_e64 v16, v1, v16, s[6:7]
	v_perm_b32 v18, v16, v10, s33
	v_pk_mul_f16 v10, v7, v14 op_sel_hi:[1,0]
	v_pk_mul_f16 v16, v11, v15 op_sel_hi:[1,0]
	v_cvt_pk_f16_f32 v138, v19, v19
	v_pk_max_f16 v10, v10, v16
	s_load_dwordx16 s[36:51], s[0:1], 0x8000
	v_cndmask_b32_e64 v16, v1, v10, s[8:9]
	v_cndmask_b32_e64 v10, v1, v10, s[10:11]
	v_perm_b32 v19, v10, v16, s33
	v_pk_mul_f16 v10, v8, v14 op_sel_hi:[1,0]
	v_pk_mul_f16 v16, v12, v15 op_sel_hi:[1,0]
	v_pk_mul_f16 v7, v7, v17 op_sel_hi:[1,0]
	v_pk_max_f16 v10, v10, v16
	v_pk_mul_f16 v11, v11, v22 op_sel_hi:[1,0]
	v_cndmask_b32_e64 v16, v1, v10, s[12:13]
	v_cndmask_b32_e64 v10, v1, v10, s[14:15]
	v_perm_b32 v20, v10, v16, s33
	v_pk_mul_f16 v10, v9, v14 op_sel_hi:[1,0]
	v_pk_mul_f16 v14, v13, v15 op_sel_hi:[1,0]
	v_pk_mul_f16 v8, v8, v17 op_sel_hi:[1,0]
	v_pk_max_f16 v10, v10, v14
	v_pk_mul_f16 v12, v12, v22 op_sel_hi:[1,0]
	v_cndmask_b32_e64 v14, v1, v10, s[16:17]
	v_cndmask_b32_e64 v10, v1, v10, s[18:19]
	v_perm_b32 v21, v10, v14, s33
	v_pk_add_f16 v10, v19, v18
	v_pk_add_f16 v14, v20, v21
	v_pk_mul_f16 v9, v9, v17 op_sel_hi:[1,0]
	v_pk_mul_f16 v13, v13, v22 op_sel_hi:[1,0]
	v_pk_add_f16 v10, v10, v14
	v_mov_b32_e32 v134, v3
	v_pk_max_f16 v7, v7, v11
	v_pk_max_f16 v8, v8, v12
	v_pk_max_f16 v9, v9, v13
	v_dot2c_f32_f16_e32 v134, 0x3c003c00, v10
	s_waitcnt lgkmcnt(0)
	v_cndmask_b32_e64 v10, v138, v6, s[36:37]
	v_cndmask_b32_e64 v6, v138, v6, s[38:39]
	v_cndmask_b32_e64 v11, v138, v7, s[40:41]
	v_cndmask_b32_e64 v7, v138, v7, s[42:43]
	v_cndmask_b32_e64 v12, v138, v8, s[44:45]
	v_cndmask_b32_e64 v8, v138, v8, s[46:47]
	v_cndmask_b32_e64 v13, v138, v9, s[48:49]
	v_cndmask_b32_e64 v9, v138, v9, s[50:51]
	v_perm_b32 v38, v6, v10, s33
	v_perm_b32 v39, v7, v11, s33
	v_perm_b32 v40, v8, v12, s33
	v_perm_b32 v41, v9, v13, s33
	v_pk_add_f16 v6, v39, v38
	v_pk_add_f16 v7, v40, v41
	v_mov_b32_e32 v135, v3
	v_pk_add_f16 v6, v6, v7
	v_mad_u32_u24 v141, v4, s34, v5
	v_dot2c_f32_f16_e32 v135, 0x3c003c00, v6
	v_or_b32_e32 v6, 0x1b020, v5
	s_load_dwordx16 s[36:51], s[0:1], 0x40
	s_load_dwordx16 s[4:19], s[0:1], 0x8040
	v_or_b32_e32 v7, 0x1b820, v5
	ds_read_b128 v[46:49], v6
	ds_read_b128 v[42:45], v7
	ds_read_b128 v[74:77], v141
	ds_read_b128 v[126:129], v141 offset:4608
	ds_read_b128 v[122:125], v141 offset:9216
	ds_read_b128 v[118:121], v141 offset:13824
	ds_read_b128 v[106:109], v141 offset:18432
	ds_read_b128 v[98:101], v141 offset:23040
	ds_read_b128 v[94:97], v141 offset:27648
	ds_read_b128 v[86:89], v141 offset:32256
	s_add_u32 s34, s52, s31
	s_addc_u32 s35, s53, 0
	s_add_u32 s94, s34, 0x10000
	s_addc_u32 s95, s35, 0
	v_lshlrev_b32_e32 v164, 4, v0
	v_add_u32_e32 v165, 0x1000, v164
	v_add_u32_e32 v166, 0x2000, v164
	v_add_u32_e32 v167, 0x3000, v164
	v_add_u32_e32 v168, 0x4000, v164
	v_add_u32_e32 v169, 0x5000, v164
	v_add_u32_e32 v170, 0x6000, v164
	v_add_u32_e32 v171, 0x7000, v164
	s_lshl_b32 s31, s2, 9
	s_lshl_b32 s28, s28, 4
	s_and_b32 s31, s31, 0xfffff000
	s_and_b32 s28, s28, 0xfffffc00
	s_add_i32 s31, s31, s28
	s_or_b32 s28, s31, s29
	s_ashr_i32 s29, s28, 31
	v_lshl_add_u64 v[2:3], s[34:35], 0, v[2:3]
	s_mov_b64 s[34:35], 0x1700c
	s_lshl_b64 s[28:29], s[28:29], 6
	v_lshl_add_u64 v[130:131], v[2:3], 0, s[34:35]
	s_add_u32 s35, s20, s28
	v_or_b32_e32 v145, 0x1b040, v5
	s_movk_i32 s34, 0xf000
	s_addc_u32 s84, s21, s29
	s_mov_b64 s[20:21], 0
	s_movk_i32 s85, 0x9000
	s_movk_i32 s86, 0xa000
	s_movk_i32 s87, 0xb000
	s_movk_i32 s88, 0xc000
	s_movk_i32 s89, 0xd000
	s_movk_i32 s90, 0xe000
	s_mov_b64 s[28:29], 0x8000
.LBB1_3:
	global_load_dwordx4 v[6:9], v164, s[94:95]
	global_load_dwordx4 v[2:5], v165, s[94:95]
	global_load_dwordx4 v[14:17], v166, s[94:95]
	global_load_dwordx4 v[10:13], v167, s[94:95]
	global_load_dwordx4 v[26:29], v168, s[94:95]
	global_load_dwordx4 v[22:25], v169, s[94:95]
	global_load_dwordx4 v[30:33], v170, s[94:95]
	global_load_dwordx4 v[34:37], v171, s[94:95]
	s_waitcnt lgkmcnt(0)
	v_mfma_f32_32x32x16_f16 a[0:15], v[18:21], v[74:77], a[0:15]
	s_add_i32 s31, s30, 1
	s_cmp_lg_u32 s30, 2
	s_cselect_b32 s91, s31, 0
	s_mul_i32 s30, s30, 0x9000
	s_mul_i32 s92, s91, 0x9000
	v_add_u32_e32 v147, s30, v141
	v_add_u32_e32 v146, s92, v141
	s_add_u32 s30, s35, s20
	s_addc_u32 s31, s84, s21
	s_load_dwordx16 s[68:83], s[30:31], 0x80
	s_load_dwordx16 s[52:67], s[30:31], 0x8080
	ds_read_b128 v[90:93], v145
	ds_read_b128 v[82:85], v145 offset:2048
	v_mfma_f32_32x32x16_f16 a[240:255], v[38:41], v[74:77], a[240:255]
	ds_read_b128 v[50:53], v147 offset:32
	v_pk_mul_f16 v148, v46, v136
	v_pk_mul_f16 v149, v42, v137
	v_pk_mul_f16 v150, v47, v136
	v_pk_mul_f16 v151, v43, v137
	v_mfma_f32_32x32x16_f16 a[16:31], v[18:21], v[126:129], a[16:31]
	ds_read_b128 v[54:57], v147 offset:4640
	v_pk_mul_f16 v152, v48, v136
	v_pk_mul_f16 v153, v44, v137
	v_pk_mul_f16 v154, v49, v136
	v_pk_mul_f16 v155, v45, v137
	v_mfma_f32_32x32x16_f16 a[224:239], v[38:41], v[126:129], a[224:239]
	ds_read_b128 v[58:61], v147 offset:9248
	v_pk_mul_f16 v156, v46, v140
	v_pk_mul_f16 v157, v42, v139
	v_pk_mul_f16 v158, v47, v140
	v_pk_mul_f16 v159, v43, v139
	v_mfma_f32_32x32x16_f16 a[32:47], v[18:21], v[122:125], a[32:47]
	ds_read_b128 v[62:65], v147 offset:13856
	v_pk_mul_f16 v160, v48, v140
	v_pk_mul_f16 v161, v44, v139
	v_pk_mul_f16 v162, v49, v140
	v_pk_mul_f16 v163, v45, v139
	v_mfma_f32_32x32x16_f16 a[208:223], v[38:41], v[122:125], a[208:223]
	ds_read_b128 v[66:69], v147 offset:18464
	v_pk_max_f16 v148, v148, v149
	v_pk_max_f16 v150, v150, v151
	v_pk_max_f16 v152, v152, v153
	v_pk_max_f16 v154, v154, v155
	v_mfma_f32_32x32x16_f16 a[48:63], v[18:21], v[118:121], a[48:63]
	ds_read_b128 v[70:73], v147 offset:23072
	v_pk_max_f16 v156, v156, v157
	v_pk_max_f16 v158, v158, v159
	v_pk_max_f16 v160, v160, v161
	v_pk_max_f16 v162, v162, v163
	v_mfma_f32_32x32x16_f16 a[192:207], v[38:41], v[118:121], a[192:207]
	ds_read_b128 v[78:81], v147 offset:27680
	v_cndmask_b32_e64 v114, v1, v148, s[36:37]
	s_mov_b64 vcc, s[38:39]
	v_cndmask_b32_sdwa v114, v1, v148, vcc dst_sel:WORD_1 dst_unused:UNUSED_PRESERVE src0_sel:WORD_1 src1_sel:WORD_1
	v_cndmask_b32_e64 v115, v1, v150, s[40:41]
	s_mov_b64 vcc, s[42:43]
	v_cndmask_b32_sdwa v115, v1, v150, vcc dst_sel:WORD_1 dst_unused:UNUSED_PRESERVE src0_sel:WORD_1 src1_sel:WORD_1
	v_mfma_f32_32x32x16_f16 a[64:79], v[18:21], v[106:109], a[64:79]
	ds_read_b128 v[102:105], v147 offset:32288
	v_cndmask_b32_e64 v116, v1, v152, s[44:45]
	s_mov_b64 vcc, s[46:47]
	v_cndmask_b32_sdwa v116, v1, v152, vcc dst_sel:WORD_1 dst_unused:UNUSED_PRESERVE src0_sel:WORD_1 src1_sel:WORD_1
	v_cndmask_b32_e64 v117, v1, v154, s[48:49]
	s_mov_b64 vcc, s[50:51]
	v_cndmask_b32_sdwa v117, v1, v154, vcc dst_sel:WORD_1 dst_unused:UNUSED_PRESERVE src0_sel:WORD_1 src1_sel:WORD_1
	v_mfma_f32_32x32x16_f16 a[176:191], v[38:41], v[106:109], a[176:191]
	v_cndmask_b32_e64 v110, v138, v156, s[4:5]
	s_mov_b64 vcc, s[6:7]
	v_cndmask_b32_sdwa v110, v138, v156, vcc dst_sel:WORD_1 dst_unused:UNUSED_PRESERVE src0_sel:WORD_1 src1_sel:WORD_1
	v_cndmask_b32_e64 v111, v138, v158, s[8:9]
	s_mov_b64 vcc, s[10:11]
	v_cndmask_b32_sdwa v111, v138, v158, vcc dst_sel:WORD_1 dst_unused:UNUSED_PRESERVE src0_sel:WORD_1 src1_sel:WORD_1
	v_mfma_f32_32x32x16_f16 a[112:127], v[18:21], v[98:101], a[112:127]
	v_cndmask_b32_e64 v112, v138, v160, s[12:13]
	s_mov_b64 vcc, s[14:15]
	v_cndmask_b32_sdwa v112, v138, v160, vcc dst_sel:WORD_1 dst_unused:UNUSED_PRESERVE src0_sel:WORD_1 src1_sel:WORD_1
	v_cndmask_b32_e64 v113, v138, v162, s[16:17]
	s_mov_b64 vcc, s[18:19]
	v_cndmask_b32_sdwa v113, v138, v162, vcc dst_sel:WORD_1 dst_unused:UNUSED_PRESERVE src0_sel:WORD_1 src1_sel:WORD_1
	v_mfma_f32_32x32x16_f16 a[160:175], v[38:41], v[98:101], a[160:175]
	v_pk_add_f16 v148, v115, v114
	v_pk_add_f16 v149, v116, v117
	v_mfma_f32_32x32x16_f16 a[128:143], v[18:21], v[94:97], a[128:143]
	v_pk_add_f16 v150, v111, v110
	v_pk_add_f16 v151, v112, v113
	v_mfma_f32_32x32x16_f16 a[144:159], v[38:41], v[94:97], a[144:159]
	v_pk_add_f16 v148, v148, v149
	v_pk_add_f16 v150, v150, v151
	v_mfma_f32_32x32x16_f16 a[80:95], v[18:21], v[86:89], a[80:95]
	v_dot2c_f32_f16_e32 v134, 0x3c003c00, v148
	v_dot2c_f32_f16_e32 v135, 0x3c003c00, v150
	v_mfma_f32_32x32x16_f16 a[96:111], v[38:41], v[86:89], a[96:111]
	s_waitcnt lgkmcnt(0)
	v_mfma_f32_32x32x16_f16 a[0:15], v[114:117], v[50:53], a[0:15]
	s_load_dwordx16 s[36:51], s[30:31], 0xc0
	s_load_dwordx16 s[4:19], s[30:31], 0x80c0
	ds_read_b128 v[46:49], v145 offset:32
	ds_read_b128 v[42:45], v145 offset:2080
	v_mfma_f32_32x32x16_f16 a[240:255], v[110:113], v[50:53], a[240:255]
	ds_read_b128 v[74:77], v147 offset:64
	v_pk_mul_f16 v148, v90, v136
	v_pk_mul_f16 v149, v82, v137
	v_pk_mul_f16 v150, v91, v136
	v_pk_mul_f16 v151, v83, v137
	v_mfma_f32_32x32x16_f16 a[16:31], v[114:117], v[54:57], a[16:31]
	ds_read_b128 v[126:129], v147 offset:4672
	v_pk_mul_f16 v152, v92, v136
	v_pk_mul_f16 v153, v84, v137
	v_pk_mul_f16 v154, v93, v136
	v_pk_mul_f16 v155, v85, v137
	v_mfma_f32_32x32x16_f16 a[224:239], v[110:113], v[54:57], a[224:239]
	ds_read_b128 v[122:125], v147 offset:9280
	v_pk_mul_f16 v156, v90, v140
	v_pk_mul_f16 v157, v82, v139
	v_pk_mul_f16 v158, v91, v140
	v_pk_mul_f16 v159, v83, v139
	v_mfma_f32_32x32x16_f16 a[32:47], v[114:117], v[58:61], a[32:47]
	ds_read_b128 v[118:121], v147 offset:13888
	v_pk_mul_f16 v160, v92, v140
	v_pk_mul_f16 v161, v84, v139
	v_pk_mul_f16 v162, v93, v140
	v_pk_mul_f16 v163, v85, v139
	v_mfma_f32_32x32x16_f16 a[208:223], v[110:113], v[58:61], a[208:223]
	ds_read_b128 v[106:109], v147 offset:18496
	v_pk_max_f16 v148, v148, v149
	v_pk_max_f16 v150, v150, v151
	v_pk_max_f16 v152, v152, v153
	v_pk_max_f16 v154, v154, v155
	v_mfma_f32_32x32x16_f16 a[48:63], v[114:117], v[62:65], a[48:63]
	ds_read_b128 v[98:101], v147 offset:23104
	v_pk_max_f16 v156, v156, v157
	v_pk_max_f16 v158, v158, v159
	v_pk_max_f16 v160, v160, v161
	v_pk_max_f16 v162, v162, v163
	v_mfma_f32_32x32x16_f16 a[192:207], v[110:113], v[62:65], a[192:207]
	ds_read_b128 v[94:97], v147 offset:27712
	v_cndmask_b32_e64 v18, v1, v148, s[68:69]
	s_mov_b64 vcc, s[70:71]
	v_cndmask_b32_sdwa v18, v1, v148, vcc dst_sel:WORD_1 dst_unused:UNUSED_PRESERVE src0_sel:WORD_1 src1_sel:WORD_1
	v_cndmask_b32_e64 v19, v1, v150, s[72:73]
	s_mov_b64 vcc, s[74:75]
	v_cndmask_b32_sdwa v19, v1, v150, vcc dst_sel:WORD_1 dst_unused:UNUSED_PRESERVE src0_sel:WORD_1 src1_sel:WORD_1
	v_mfma_f32_32x32x16_f16 a[64:79], v[114:117], v[66:69], a[64:79]
	ds_read_b128 v[86:89], v147 offset:32320
	v_cndmask_b32_e64 v20, v1, v152, s[76:77]
	s_mov_b64 vcc, s[78:79]
	v_cndmask_b32_sdwa v20, v1, v152, vcc dst_sel:WORD_1 dst_unused:UNUSED_PRESERVE src0_sel:WORD_1 src1_sel:WORD_1
	v_cndmask_b32_e64 v21, v1, v154, s[80:81]
	s_mov_b64 vcc, s[82:83]
	v_cndmask_b32_sdwa v21, v1, v154, vcc dst_sel:WORD_1 dst_unused:UNUSED_PRESERVE src0_sel:WORD_1 src1_sel:WORD_1
	v_mfma_f32_32x32x16_f16 a[176:191], v[110:113], v[66:69], a[176:191]
	v_cndmask_b32_e64 v38, v138, v156, s[52:53]
	s_mov_b64 vcc, s[54:55]
	v_cndmask_b32_sdwa v38, v138, v156, vcc dst_sel:WORD_1 dst_unused:UNUSED_PRESERVE src0_sel:WORD_1 src1_sel:WORD_1
	v_cndmask_b32_e64 v39, v138, v158, s[56:57]
	s_mov_b64 vcc, s[58:59]
	v_cndmask_b32_sdwa v39, v138, v158, vcc dst_sel:WORD_1 dst_unused:UNUSED_PRESERVE src0_sel:WORD_1 src1_sel:WORD_1
	v_mfma_f32_32x32x16_f16 a[112:127], v[114:117], v[70:73], a[112:127]
	v_cndmask_b32_e64 v40, v138, v160, s[60:61]
	s_mov_b64 vcc, s[62:63]
	v_cndmask_b32_sdwa v40, v138, v160, vcc dst_sel:WORD_1 dst_unused:UNUSED_PRESERVE src0_sel:WORD_1 src1_sel:WORD_1
	v_cndmask_b32_e64 v41, v138, v162, s[64:65]
	s_mov_b64 vcc, s[66:67]
	v_cndmask_b32_sdwa v41, v138, v162, vcc dst_sel:WORD_1 dst_unused:UNUSED_PRESERVE src0_sel:WORD_1 src1_sel:WORD_1
	v_mfma_f32_32x32x16_f16 a[160:175], v[110:113], v[70:73], a[160:175]
	v_pk_add_f16 v148, v19, v18
	v_pk_add_f16 v149, v20, v21
	v_mfma_f32_32x32x16_f16 a[128:143], v[114:117], v[78:81], a[128:143]
	v_pk_add_f16 v150, v39, v38
	v_pk_add_f16 v151, v40, v41
	v_mfma_f32_32x32x16_f16 a[144:159], v[110:113], v[78:81], a[144:159]
	v_pk_add_f16 v148, v148, v149
	v_pk_add_f16 v150, v150, v151
	v_mfma_f32_32x32x16_f16 a[80:95], v[114:117], v[102:105], a[80:95]
	v_dot2c_f32_f16_e32 v134, 0x3c003c00, v148
	v_dot2c_f32_f16_e32 v135, 0x3c003c00, v150
	v_mfma_f32_32x32x16_f16 a[96:111], v[110:113], v[102:105], a[96:111]
	s_waitcnt lgkmcnt(0)
	v_mfma_f32_32x32x16_f16 a[0:15], v[18:21], v[74:77], a[0:15]
	s_load_dwordx16 s[68:83], s[30:31], 0x100
	s_load_dwordx16 s[52:67], s[30:31], 0x8100
	ds_read_b128 v[90:93], v145 offset:64
	ds_read_b128 v[82:85], v145 offset:2112
	v_mfma_f32_32x32x16_f16 a[240:255], v[38:41], v[74:77], a[240:255]
	ds_read_b128 v[50:53], v147 offset:96
	v_pk_mul_f16 v148, v46, v136
	v_pk_mul_f16 v149, v42, v137
	v_pk_mul_f16 v150, v47, v136
	v_pk_mul_f16 v151, v43, v137
	v_mfma_f32_32x32x16_f16 a[16:31], v[18:21], v[126:129], a[16:31]
	ds_read_b128 v[54:57], v147 offset:4704
	v_pk_mul_f16 v152, v48, v136
	v_pk_mul_f16 v153, v44, v137
	v_pk_mul_f16 v154, v49, v136
	v_pk_mul_f16 v155, v45, v137
	v_mfma_f32_32x32x16_f16 a[224:239], v[38:41], v[126:129], a[224:239]
	ds_read_b128 v[58:61], v147 offset:9312
	v_pk_mul_f16 v156, v46, v140
	v_pk_mul_f16 v157, v42, v139
	v_pk_mul_f16 v158, v47, v140
	v_pk_mul_f16 v159, v43, v139
	v_mfma_f32_32x32x16_f16 a[32:47], v[18:21], v[122:125], a[32:47]
	ds_read_b128 v[62:65], v147 offset:13920
	v_pk_mul_f16 v160, v48, v140
	v_pk_mul_f16 v161, v44, v139
	v_pk_mul_f16 v162, v49, v140
	v_pk_mul_f16 v163, v45, v139
	v_mfma_f32_32x32x16_f16 a[208:223], v[38:41], v[122:125], a[208:223]
	ds_read_b128 v[66:69], v147 offset:18528
	v_pk_max_f16 v148, v148, v149
	v_pk_max_f16 v150, v150, v151
	v_pk_max_f16 v152, v152, v153
	v_pk_max_f16 v154, v154, v155
	v_mfma_f32_32x32x16_f16 a[48:63], v[18:21], v[118:121], a[48:63]
	ds_read_b128 v[70:73], v147 offset:23136
	v_pk_max_f16 v156, v156, v157
	v_pk_max_f16 v158, v158, v159
	v_pk_max_f16 v160, v160, v161
	v_pk_max_f16 v162, v162, v163
	v_mfma_f32_32x32x16_f16 a[192:207], v[38:41], v[118:121], a[192:207]
	ds_read_b128 v[78:81], v147 offset:27744
	v_cndmask_b32_e64 v114, v1, v148, s[36:37]
	s_mov_b64 vcc, s[38:39]
	v_cndmask_b32_sdwa v114, v1, v148, vcc dst_sel:WORD_1 dst_unused:UNUSED_PRESERVE src0_sel:WORD_1 src1_sel:WORD_1
	v_cndmask_b32_e64 v115, v1, v150, s[40:41]
	s_mov_b64 vcc, s[42:43]
	v_cndmask_b32_sdwa v115, v1, v150, vcc dst_sel:WORD_1 dst_unused:UNUSED_PRESERVE src0_sel:WORD_1 src1_sel:WORD_1
	v_mfma_f32_32x32x16_f16 a[64:79], v[18:21], v[106:109], a[64:79]
	ds_read_b128 v[102:105], v147 offset:32352
	v_cndmask_b32_e64 v116, v1, v152, s[44:45]
	s_mov_b64 vcc, s[46:47]
	v_cndmask_b32_sdwa v116, v1, v152, vcc dst_sel:WORD_1 dst_unused:UNUSED_PRESERVE src0_sel:WORD_1 src1_sel:WORD_1
	v_cndmask_b32_e64 v117, v1, v154, s[48:49]
	s_mov_b64 vcc, s[50:51]
	v_cndmask_b32_sdwa v117, v1, v154, vcc dst_sel:WORD_1 dst_unused:UNUSED_PRESERVE src0_sel:WORD_1 src1_sel:WORD_1
	v_mfma_f32_32x32x16_f16 a[176:191], v[38:41], v[106:109], a[176:191]
	v_cndmask_b32_e64 v110, v138, v156, s[4:5]
	s_mov_b64 vcc, s[6:7]
	v_cndmask_b32_sdwa v110, v138, v156, vcc dst_sel:WORD_1 dst_unused:UNUSED_PRESERVE src0_sel:WORD_1 src1_sel:WORD_1
	v_cndmask_b32_e64 v111, v138, v158, s[8:9]
	s_mov_b64 vcc, s[10:11]
	v_cndmask_b32_sdwa v111, v138, v158, vcc dst_sel:WORD_1 dst_unused:UNUSED_PRESERVE src0_sel:WORD_1 src1_sel:WORD_1
	v_mfma_f32_32x32x16_f16 a[112:127], v[18:21], v[98:101], a[112:127]
	v_cndmask_b32_e64 v112, v138, v160, s[12:13]
	s_mov_b64 vcc, s[14:15]
	v_cndmask_b32_sdwa v112, v138, v160, vcc dst_sel:WORD_1 dst_unused:UNUSED_PRESERVE src0_sel:WORD_1 src1_sel:WORD_1
	v_cndmask_b32_e64 v113, v138, v162, s[16:17]
	s_mov_b64 vcc, s[18:19]
	v_cndmask_b32_sdwa v113, v138, v162, vcc dst_sel:WORD_1 dst_unused:UNUSED_PRESERVE src0_sel:WORD_1 src1_sel:WORD_1
	v_mfma_f32_32x32x16_f16 a[160:175], v[38:41], v[98:101], a[160:175]
	v_pk_add_f16 v148, v115, v114
	v_pk_add_f16 v149, v116, v117
	v_mfma_f32_32x32x16_f16 a[128:143], v[18:21], v[94:97], a[128:143]
	v_pk_add_f16 v150, v111, v110
	v_pk_add_f16 v151, v112, v113
	v_mfma_f32_32x32x16_f16 a[144:159], v[38:41], v[94:97], a[144:159]
	v_pk_add_f16 v148, v148, v149
	v_pk_add_f16 v150, v150, v151
	v_mfma_f32_32x32x16_f16 a[80:95], v[18:21], v[86:89], a[80:95]
	v_dot2c_f32_f16_e32 v134, 0x3c003c00, v148
	v_dot2c_f32_f16_e32 v135, 0x3c003c00, v150
	v_mfma_f32_32x32x16_f16 a[96:111], v[38:41], v[86:89], a[96:111]
	s_waitcnt lgkmcnt(0)
	v_mfma_f32_32x32x16_f16 a[0:15], v[114:117], v[50:53], a[0:15]
	s_load_dwordx16 s[36:51], s[30:31], 0x140
	s_load_dwordx16 s[4:19], s[30:31], 0x8140
	ds_read_b128 v[46:49], v145 offset:96
	ds_read_b128 v[42:45], v145 offset:2144
	v_mfma_f32_32x32x16_f16 a[240:255], v[110:113], v[50:53], a[240:255]
	ds_read_b128 v[74:77], v146
	v_pk_mul_f16 v148, v90, v136
	v_pk_mul_f16 v149, v82, v137
	v_pk_mul_f16 v150, v91, v136
	v_pk_mul_f16 v151, v83, v137
	v_mfma_f32_32x32x16_f16 a[16:31], v[114:117], v[54:57], a[16:31]
	ds_read_b128 v[126:129], v146 offset:4608
	v_pk_mul_f16 v152, v92, v136
	v_pk_mul_f16 v153, v84, v137
	v_pk_mul_f16 v154, v93, v136
	v_pk_mul_f16 v155, v85, v137
	v_mfma_f32_32x32x16_f16 a[224:239], v[110:113], v[54:57], a[224:239]
	ds_read_b128 v[122:125], v146 offset:9216
	v_pk_mul_f16 v156, v90, v140
	v_pk_mul_f16 v157, v82, v139
	v_pk_mul_f16 v158, v91, v140
	v_pk_mul_f16 v159, v83, v139
	v_mfma_f32_32x32x16_f16 a[32:47], v[114:117], v[58:61], a[32:47]
	ds_read_b128 v[118:121], v146 offset:13824
	v_pk_mul_f16 v160, v92, v140
	v_pk_mul_f16 v161, v84, v139
	v_pk_mul_f16 v162, v93, v140
	v_pk_mul_f16 v163, v85, v139
	v_mfma_f32_32x32x16_f16 a[208:223], v[110:113], v[58:61], a[208:223]
	ds_read_b128 v[106:109], v146 offset:18432
	v_pk_max_f16 v148, v148, v149
	v_pk_max_f16 v150, v150, v151
	v_pk_max_f16 v152, v152, v153
	v_pk_max_f16 v154, v154, v155
	v_mfma_f32_32x32x16_f16 a[48:63], v[114:117], v[62:65], a[48:63]
	ds_read_b128 v[98:101], v146 offset:23040
	v_pk_max_f16 v156, v156, v157
	v_pk_max_f16 v158, v158, v159
	v_pk_max_f16 v160, v160, v161
	v_pk_max_f16 v162, v162, v163
	v_mfma_f32_32x32x16_f16 a[192:207], v[110:113], v[62:65], a[192:207]
	ds_read_b128 v[94:97], v146 offset:27648
	v_cndmask_b32_e64 v18, v1, v148, s[68:69]
	s_mov_b64 vcc, s[70:71]
	v_cndmask_b32_sdwa v18, v1, v148, vcc dst_sel:WORD_1 dst_unused:UNUSED_PRESERVE src0_sel:WORD_1 src1_sel:WORD_1
	v_cndmask_b32_e64 v19, v1, v150, s[72:73]
	s_mov_b64 vcc, s[74:75]
	v_cndmask_b32_sdwa v19, v1, v150, vcc dst_sel:WORD_1 dst_unused:UNUSED_PRESERVE src0_sel:WORD_1 src1_sel:WORD_1
	v_mfma_f32_32x32x16_f16 a[64:79], v[114:117], v[66:69], a[64:79]
	ds_read_b128 v[86:89], v146 offset:32256
	v_cndmask_b32_e64 v20, v1, v152, s[76:77]
	s_mov_b64 vcc, s[78:79]
	v_cndmask_b32_sdwa v20, v1, v152, vcc dst_sel:WORD_1 dst_unused:UNUSED_PRESERVE src0_sel:WORD_1 src1_sel:WORD_1
	v_cndmask_b32_e64 v21, v1, v154, s[80:81]
	s_mov_b64 vcc, s[82:83]
	v_cndmask_b32_sdwa v21, v1, v154, vcc dst_sel:WORD_1 dst_unused:UNUSED_PRESERVE src0_sel:WORD_1 src1_sel:WORD_1
	v_mfma_f32_32x32x16_f16 a[176:191], v[110:113], v[66:69], a[176:191]
	v_cndmask_b32_e64 v38, v138, v156, s[52:53]
	s_mov_b64 vcc, s[54:55]
	v_cndmask_b32_sdwa v38, v138, v156, vcc dst_sel:WORD_1 dst_unused:UNUSED_PRESERVE src0_sel:WORD_1 src1_sel:WORD_1
	v_cndmask_b32_e64 v39, v138, v158, s[56:57]
	s_mov_b64 vcc, s[58:59]
	v_cndmask_b32_sdwa v39, v138, v158, vcc dst_sel:WORD_1 dst_unused:UNUSED_PRESERVE src0_sel:WORD_1 src1_sel:WORD_1
	v_mfma_f32_32x32x16_f16 a[112:127], v[114:117], v[70:73], a[112:127]
	v_cndmask_b32_e64 v40, v138, v160, s[60:61]
	s_mov_b64 vcc, s[62:63]
	v_cndmask_b32_sdwa v40, v138, v160, vcc dst_sel:WORD_1 dst_unused:UNUSED_PRESERVE src0_sel:WORD_1 src1_sel:WORD_1
	v_cndmask_b32_e64 v41, v138, v162, s[64:65]
	s_mov_b64 vcc, s[66:67]
	v_cndmask_b32_sdwa v41, v138, v162, vcc dst_sel:WORD_1 dst_unused:UNUSED_PRESERVE src0_sel:WORD_1 src1_sel:WORD_1
	v_mfma_f32_32x32x16_f16 a[160:175], v[110:113], v[70:73], a[160:175]
	v_pk_add_f16 v148, v19, v18
	v_pk_add_f16 v149, v20, v21
	v_mfma_f32_32x32x16_f16 a[128:143], v[114:117], v[78:81], a[128:143]
	v_pk_add_f16 v150, v39, v38
	v_pk_add_f16 v151, v40, v41
	v_mfma_f32_32x32x16_f16 a[144:159], v[110:113], v[78:81], a[144:159]
	v_pk_add_f16 v148, v148, v149
	v_pk_add_f16 v150, v150, v151
	v_mfma_f32_32x32x16_f16 a[80:95], v[114:117], v[102:105], a[80:95]
	v_dot2c_f32_f16_e32 v134, 0x3c003c00, v148
	v_dot2c_f32_f16_e32 v135, 0x3c003c00, v150
	v_mfma_f32_32x32x16_f16 a[96:111], v[110:113], v[102:105], a[96:111]
	s_add_i32 s92, s92, 0x9000
	s_cmp_lg_u32 s91, 2
	s_cselect_b32 s30, s92, 0
	s_add_u32 s20, s20, 0x100
	s_addc_u32 s21, s21, 0
	v_add_u32_e32 v50, s30, v144
	s_add_u32 s94, s94, 0x8000
	s_addc_u32 s95, s95, 0
	v_add_u32_e32 v145, 0x80, v145
	s_cmpk_eq_i32 s20, 0xf00
	s_mov_b32 s30, s91
	s_waitcnt vmcnt(6)
	s_waitcnt vmcnt(5)
	s_waitcnt vmcnt(4)
	s_waitcnt vmcnt(3)
	s_waitcnt vmcnt(2)
	s_waitcnt vmcnt(1)
	s_waitcnt vmcnt(0)
	ds_write_b128 v50, v[6:9]
	ds_write_b128 v50, v[2:5] offset:4608
	ds_write_b128 v50, v[14:17] offset:9216
	ds_write_b128 v50, v[10:13] offset:13824
	ds_write_b128 v50, v[26:29] offset:18432
	ds_write_b128 v50, v[22:25] offset:23040
	ds_write_b128 v50, v[30:33] offset:27648
	ds_write_b128 v50, v[34:37] offset:32256
	s_waitcnt lgkmcnt(0)
	s_barrier
	s_cbranch_scc0 .LBB1_3
	v_accvgpr_read_b32 v175, a95
	v_accvgpr_read_b32 v174, a94
	v_accvgpr_read_b32 v173, a93
	v_accvgpr_read_b32 v172, a92
	v_accvgpr_read_b32 v171, a91
	v_accvgpr_read_b32 v170, a90
	v_accvgpr_read_b32 v169, a89
	v_accvgpr_read_b32 v168, a88
	v_accvgpr_read_b32 v167, a87
	v_accvgpr_read_b32 v166, a86
	v_accvgpr_read_b32 v165, a85
	v_accvgpr_read_b32 v164, a84
	v_accvgpr_read_b32 v163, a83
	v_accvgpr_read_b32 v162, a82
	v_accvgpr_read_b32 v161, a81
	v_accvgpr_read_b32 v160, a80
	v_mfma_f32_32x32x16_f16 a[80:95], v[18:21], v[74:77], a[0:15]
	s_nop 11
	v_accvgpr_read_b32 v159, a95
	v_accvgpr_read_b32 v158, a94
	v_accvgpr_read_b32 v157, a93
	v_accvgpr_read_b32 v156, a92
	v_accvgpr_read_b32 v155, a91
	v_accvgpr_read_b32 v154, a90
	v_accvgpr_read_b32 v153, a89
	v_accvgpr_read_b32 v152, a88
	v_accvgpr_read_b32 v151, a87
	v_accvgpr_read_b32 v150, a86
	v_accvgpr_read_b32 v149, a85
	v_accvgpr_read_b32 v148, a84
	v_accvgpr_read_b32 v147, a83
	v_accvgpr_read_b32 v146, a82
	v_accvgpr_read_b32 v145, a81
	v_accvgpr_read_b32 v144, a80
	ds_read_b128 v[2:5], v141 offset:32288
	ds_read_b128 v[82:85], v141 offset:32
	ds_read_b128 v[58:61], v141 offset:4640
	ds_read_b128 v[50:53], v141 offset:9248
	ds_read_b128 v[26:29], v141 offset:13856
	ds_read_b128 v[22:25], v141 offset:18464
	ds_read_b128 v[14:17], v141 offset:23072
	ds_read_b128 v[10:13], v141 offset:27680
	s_load_dwordx16 s[68:83], s[0:1], 0xf80
	s_load_dwordx16 s[52:67], s[0:1], 0x8f80
	ds_read_b128 v[54:57], v142 offset:1984
	ds_read_b128 v[34:37], v143 offset:1984
	v_mfma_f32_32x32x16_f16 a[0:15], v[38:41], v[74:77], a[240:255]
	v_pk_mul_f16 v6, v46, v136
	v_pk_mul_f16 v7, v42, v137
	s_mov_b32 s20, 0x7060100
	v_pk_max_f16 v6, v6, v7
	s_nop 0
	v_cndmask_b32_e64 v7, v1, v6, s[36:37]
	v_mfma_f32_32x32x16_f16 a[240:255], v[18:21], v[126:129], a[16:31]
	v_cndmask_b32_e64 v6, v1, v6, s[38:39]
	v_perm_b32 v74, v6, v7, s20
	v_pk_mul_f16 v6, v47, v136
	v_pk_mul_f16 v7, v43, v137
	v_mfma_f32_32x32x16_f16 a[16:31], v[38:41], v[126:129], a[224:239]
	v_pk_max_f16 v6, v6, v7
	s_nop 0
	v_cndmask_b32_e64 v7, v1, v6, s[40:41]
	v_cndmask_b32_e64 v6, v1, v6, s[42:43]
	v_perm_b32 v75, v6, v7, s20
	v_mfma_f32_32x32x16_f16 a[224:239], v[18:21], v[122:125], a[32:47]
	v_pk_mul_f16 v6, v48, v136
	v_pk_mul_f16 v7, v44, v137
	s_nop 0
	v_pk_max_f16 v6, v6, v7
	s_nop 0
	v_cndmask_b32_e64 v7, v1, v6, s[44:45]
	v_mfma_f32_32x32x16_f16 a[32:47], v[38:41], v[122:125], a[208:223]
	v_cndmask_b32_e64 v6, v1, v6, s[46:47]
	v_perm_b32 v76, v6, v7, s20
	v_pk_mul_f16 v6, v49, v136
	v_pk_mul_f16 v7, v45, v137
	v_mfma_f32_32x32x16_f16 a[208:223], v[18:21], v[118:121], a[48:63]
	v_pk_max_f16 v6, v6, v7
	s_nop 0
	v_cndmask_b32_e64 v7, v1, v6, s[48:49]
	v_cndmask_b32_e64 v6, v1, v6, s[50:51]
	v_perm_b32 v77, v6, v7, s20
	v_mfma_f32_32x32x16_f16 a[48:63], v[38:41], v[118:121], a[192:207]
	v_pk_add_f16 v6, v75, v74
	v_pk_add_f16 v7, v76, v77
	s_nop 0
	v_pk_add_f16 v6, v6, v7
	s_nop 0
	v_dot2c_f32_f16_e32 v134, 0x3c003c00, v6
	v_mfma_f32_32x32x16_f16 a[192:207], v[18:21], v[106:109], a[64:79]
	v_pk_mul_f16 v6, v46, v140
	v_pk_mul_f16 v7, v42, v139
	s_nop 0
	v_pk_max_f16 v6, v6, v7
	s_nop 0
	v_cndmask_b32_e64 v7, v138, v6, s[4:5]
	v_mfma_f32_32x32x16_f16 a[64:79], v[38:41], v[106:109], a[176:191]
	v_pk_mul_f16 v8, v47, v140
	v_pk_mul_f16 v9, v43, v139
	v_cndmask_b32_e64 v6, v138, v6, s[6:7]
	v_pk_max_f16 v8, v8, v9
	v_mfma_f32_32x32x16_f16 a[176:191], v[18:21], v[98:101], a[112:127]
	v_pk_mul_f16 v30, v48, v140
	v_pk_mul_f16 v31, v44, v139
	v_cndmask_b32_e64 v9, v138, v8, s[8:9]
	v_cndmask_b32_e64 v8, v138, v8, s[10:11]
	v_mfma_f32_32x32x16_f16 a[112:127], v[38:41], v[98:101], a[160:175]
	v_pk_max_f16 v30, v30, v31
	v_pk_mul_f16 v32, v49, v140
	v_cndmask_b32_e64 v31, v138, v30, s[12:13]
	v_cndmask_b32_e64 v30, v138, v30, s[14:15]
	v_mfma_f32_32x32x16_f16 a[160:175], v[18:21], v[94:97], a[128:143]
	v_pk_mul_f16 v33, v45, v139
	s_nop 0
	v_pk_max_f16 v32, v32, v33
	s_nop 0
	v_cndmask_b32_e64 v33, v138, v32, s[16:17]
	v_cndmask_b32_e64 v32, v138, v32, s[18:19]
	v_mfma_f32_32x32x16_f16 a[128:143], v[38:41], v[94:97], a[144:159]
	v_perm_b32 v78, v6, v7, s20
	v_perm_b32 v79, v8, v9, s20
	v_perm_b32 v80, v30, v31, s20
	v_perm_b32 v81, v32, v33, s20
	v_pk_add_f16 v6, v79, v78
	v_pk_add_f16 v7, v80, v81
	v_accvgpr_write_b32 a80, v160
	v_pk_add_f16 v6, v6, v7
	v_accvgpr_write_b32 a81, v161
	v_accvgpr_write_b32 a82, v162
	v_accvgpr_write_b32 a83, v163
	v_accvgpr_write_b32 a84, v164
	v_accvgpr_write_b32 a85, v165
	v_accvgpr_write_b32 a86, v166
	v_accvgpr_write_b32 a87, v167
	v_accvgpr_write_b32 a88, v168
	v_accvgpr_write_b32 a89, v169
	v_accvgpr_write_b32 a90, v170
	v_accvgpr_write_b32 a91, v171
	v_accvgpr_write_b32 a92, v172
	v_accvgpr_write_b32 a93, v173
	v_accvgpr_write_b32 a94, v174
	v_accvgpr_write_b32 a95, v175
	v_dot2c_f32_f16_e32 v135, 0x3c003c00, v6
	s_nop 0
	v_mfma_f32_32x32x16_f16 a[144:159], v[18:21], v[86:89], a[80:95]
	v_mfma_f32_32x32x16_f16 a[80:95], v[38:41], v[86:89], a[96:111]
	s_nop 6
	v_accvgpr_write_b32 a96, v144
	v_accvgpr_write_b32 a97, v145
	v_accvgpr_write_b32 a98, v146
	v_accvgpr_write_b32 a99, v147
	v_accvgpr_write_b32 a100, v148
	v_accvgpr_write_b32 a101, v149
	v_accvgpr_write_b32 a102, v150
	v_accvgpr_write_b32 a103, v151
	v_accvgpr_write_b32 a104, v152
	v_accvgpr_write_b32 a105, v153
	v_accvgpr_write_b32 a106, v154
	v_accvgpr_write_b32 a107, v155
	v_accvgpr_write_b32 a108, v156
	v_accvgpr_write_b32 a109, v157
	v_accvgpr_write_b32 a110, v158
	v_accvgpr_write_b32 a111, v159
	s_waitcnt lgkmcnt(0)
	s_nop 0
	v_mfma_f32_32x32x16_f16 a[96:111], v[74:77], v[82:85], a[96:111]
	ds_read_b128 v[86:89], v141 offset:64
	ds_read_b128 v[70:73], v141 offset:4672
	ds_read_b128 v[62:65], v141 offset:9280
	ds_read_b128 v[42:45], v141 offset:13888
	ds_read_b128 v[38:41], v141 offset:18496
	ds_read_b128 v[30:33], v141 offset:23104
	ds_read_b128 v[18:21], v141 offset:27712
	ds_read_b128 v[6:9], v141 offset:32320
	s_load_dwordx16 s[36:51], s[0:1], 0xfc0
	s_load_dwordx16 s[4:19], s[0:1], 0x8fc0
	ds_read_b128 v[66:69], v142 offset:2016
	ds_read_b128 v[46:49], v143 offset:2016
	v_mfma_f32_32x32x16_f16 a[0:15], v[78:81], v[82:85], a[0:15]
	v_pk_mul_f16 v82, v54, v136
	v_pk_mul_f16 v83, v34, v137
	s_nop 0
	v_pk_max_f16 v82, v82, v83
	s_nop 0
	v_cndmask_b32_e64 v83, v1, v82, s[68:69]
	v_mfma_f32_32x32x16_f16 a[240:255], v[74:77], v[58:61], a[240:255]
	v_cndmask_b32_e64 v82, v1, v82, s[70:71]
	v_perm_b32 v82, v82, v83, s20
	v_pk_mul_f16 v83, v55, v136
	v_pk_mul_f16 v84, v35, v137
	v_mfma_f32_32x32x16_f16 a[16:31], v[78:81], v[58:61], a[16:31]
	v_pk_max_f16 v58, v83, v84
	s_nop 0
	v_cndmask_b32_e64 v59, v1, v58, s[72:73]
	v_cndmask_b32_e64 v58, v1, v58, s[74:75]
	v_perm_b32 v83, v58, v59, s20
	v_mfma_f32_32x32x16_f16 a[224:239], v[74:77], v[50:53], a[224:239]
	v_pk_mul_f16 v58, v56, v136
	v_pk_mul_f16 v59, v36, v137
	s_nop 0
	v_pk_max_f16 v58, v58, v59
	s_nop 0
	v_cndmask_b32_e64 v59, v1, v58, s[76:77]
	v_mfma_f32_32x32x16_f16 a[32:47], v[78:81], v[50:53], a[32:47]
	v_cndmask_b32_e64 v50, v1, v58, s[78:79]
	v_perm_b32 v84, v50, v59, s20
	v_pk_mul_f16 v50, v57, v136
	v_pk_mul_f16 v51, v37, v137
	v_mfma_f32_32x32x16_f16 a[208:223], v[74:77], v[26:29], a[208:223]
	v_pk_max_f16 v50, v50, v51
	s_nop 0
	v_cndmask_b32_e64 v51, v1, v50, s[80:81]
	v_cndmask_b32_e64 v50, v1, v50, s[82:83]
	v_perm_b32 v85, v50, v51, s20
	v_mfma_f32_32x32x16_f16 a[48:63], v[78:81], v[26:29], a[48:63]
	v_pk_add_f16 v26, v83, v82
	v_pk_add_f16 v27, v84, v85
	s_nop 0
	v_pk_add_f16 v26, v26, v27
	s_nop 0
	v_dot2c_f32_f16_e32 v134, 0x3c003c00, v26
	v_mfma_f32_32x32x16_f16 a[192:207], v[74:77], v[22:25], a[192:207]
	v_pk_mul_f16 v26, v54, v140
	v_pk_mul_f16 v27, v34, v139
	s_nop 0
	v_pk_max_f16 v26, v26, v27
	s_nop 0
	v_cndmask_b32_e64 v27, v138, v26, s[52:53]
	v_mfma_f32_32x32x16_f16 a[64:79], v[78:81], v[22:25], a[64:79]
	v_pk_mul_f16 v23, v55, v140
	v_pk_mul_f16 v24, v35, v139
	v_cndmask_b32_e64 v22, v138, v26, s[54:55]
	v_pk_max_f16 v23, v23, v24
	v_mfma_f32_32x32x16_f16 a[176:191], v[74:77], v[14:17], a[176:191]
	v_pk_mul_f16 v25, v56, v140
	v_pk_mul_f16 v26, v36, v139
	v_cndmask_b32_e64 v24, v138, v23, s[56:57]
	v_cndmask_b32_e64 v23, v138, v23, s[58:59]
	v_mfma_f32_32x32x16_f16 a[112:127], v[78:81], v[14:17], a[112:127]
	v_pk_max_f16 v14, v25, v26
	v_pk_mul_f16 v16, v57, v140
	v_cndmask_b32_e64 v15, v138, v14, s[60:61]
	v_cndmask_b32_e64 v14, v138, v14, s[62:63]
	v_mfma_f32_32x32x16_f16 a[160:175], v[74:77], v[10:13], a[160:175]
	v_pk_mul_f16 v17, v37, v139
	s_nop 0
	v_pk_max_f16 v16, v16, v17
	s_nop 0
	v_cndmask_b32_e64 v17, v138, v16, s[64:65]
	v_cndmask_b32_e64 v16, v138, v16, s[66:67]
	v_mfma_f32_32x32x16_f16 a[128:143], v[78:81], v[10:13], a[128:143]
	v_perm_b32 v10, v22, v27, s20
	v_perm_b32 v11, v23, v24, s20
	v_perm_b32 v12, v14, v15, s20
	v_perm_b32 v13, v16, v17, s20
	v_mfma_f32_32x32x16_f16 a[144:159], v[74:77], v[2:5], a[144:159]
	v_pk_add_f16 v14, v11, v10
	v_pk_add_f16 v15, v12, v13
	s_nop 0
	v_pk_add_f16 v14, v14, v15
	s_nop 0
	v_dot2c_f32_f16_e32 v135, 0x3c003c00, v14
	v_mfma_f32_32x32x16_f16 a[80:95], v[78:81], v[2:5], a[80:95]
	s_waitcnt lgkmcnt(0)
	v_mfma_f32_32x32x16_f16 a[96:111], v[82:85], v[86:89], a[96:111]
	ds_read_b128 v[2:5], v141 offset:96
	ds_read_b128 v[14:17], v141 offset:4704
	ds_read_b128 v[22:25], v141 offset:9312
	ds_read_b128 v[26:29], v141 offset:13920
	ds_read_b128 v[34:37], v141 offset:18528
	ds_read_b128 v[50:53], v141 offset:23136
	ds_read_b128 v[54:57], v141 offset:27744
	ds_read_b128 v[58:61], v141 offset:32352
	v_mfma_f32_32x32x16_f16 a[0:15], v[10:13], v[86:89], a[0:15]
	v_pk_mul_f16 v74, v136, v66
	v_pk_mul_f16 v75, v137, v46
	s_nop 0
	v_pk_max_f16 v74, v74, v75
	s_nop 0
	v_cndmask_b32_e64 v75, v1, v74, s[36:37]
	v_mfma_f32_32x32x16_f16 a[240:255], v[82:85], v[70:73], a[240:255]
	v_cndmask_b32_e64 v74, v1, v74, s[38:39]
	v_perm_b32 v74, v74, v75, s20
	v_pk_mul_f16 v75, v136, v67
	v_pk_mul_f16 v76, v137, v47
	v_mfma_f32_32x32x16_f16 a[16:31], v[10:13], v[70:73], a[16:31]
	v_pk_max_f16 v70, v75, v76
	s_nop 0
	v_cndmask_b32_e64 v71, v1, v70, s[40:41]
	v_cndmask_b32_e64 v70, v1, v70, s[42:43]
	v_perm_b32 v75, v70, v71, s20
	v_mfma_f32_32x32x16_f16 a[224:239], v[82:85], v[62:65], a[224:239]
	v_pk_mul_f16 v70, v136, v68
	v_pk_mul_f16 v71, v137, v48
	s_nop 0
	v_pk_max_f16 v70, v70, v71
	s_nop 0
	v_cndmask_b32_e64 v71, v1, v70, s[44:45]
	v_mfma_f32_32x32x16_f16 a[32:47], v[10:13], v[62:65], a[32:47]
	v_cndmask_b32_e64 v62, v1, v70, s[46:47]
	v_perm_b32 v76, v62, v71, s20
	v_pk_mul_f16 v62, v136, v69
	v_pk_mul_f16 v63, v137, v49
	v_mfma_f32_32x32x16_f16 a[208:223], v[82:85], v[42:45], a[208:223]
	v_pk_max_f16 v62, v62, v63
	s_nop 0
	v_cndmask_b32_e64 v63, v1, v62, s[48:49]
	v_cndmask_b32_e64 v1, v1, v62, s[50:51]
	v_perm_b32 v77, v1, v63, s20
	v_mfma_f32_32x32x16_f16 a[48:63], v[10:13], v[42:45], a[48:63]
	v_pk_add_f16 v1, v75, v74
	v_pk_add_f16 v42, v76, v77
	s_nop 0
	v_pk_add_f16 v1, v1, v42
	s_nop 0
	v_dot2c_f32_f16_e32 v134, 0x3c003c00, v1
	v_mfma_f32_32x32x16_f16 a[192:207], v[82:85], v[38:41], a[192:207]
	v_pk_mul_f16 v1, v140, v66
	v_pk_mul_f16 v42, v139, v46
	s_nop 0
	v_pk_max_f16 v1, v1, v42
	s_nop 0
	v_cndmask_b32_e64 v42, v138, v1, s[4:5]
	v_mfma_f32_32x32x16_f16 a[64:79], v[10:13], v[38:41], a[64:79]
	v_pk_mul_f16 v38, v140, v67
	v_pk_mul_f16 v39, v139, v47
	v_cndmask_b32_e64 v1, v138, v1, s[6:7]
	v_pk_max_f16 v38, v38, v39
	v_mfma_f32_32x32x16_f16 a[176:191], v[82:85], v[30:33], a[176:191]
	v_pk_mul_f16 v40, v140, v68
	v_pk_mul_f16 v41, v139, v48
	v_cndmask_b32_e64 v39, v138, v38, s[8:9]
	v_cndmask_b32_e64 v38, v138, v38, s[10:11]
	v_mfma_f32_32x32x16_f16 a[112:127], v[10:13], v[30:33], a[112:127]
	v_pk_max_f16 v30, v40, v41
	v_pk_mul_f16 v32, v140, v69
	v_cndmask_b32_e64 v31, v138, v30, s[12:13]
	v_cndmask_b32_e64 v30, v138, v30, s[14:15]
	v_mfma_f32_32x32x16_f16 a[160:175], v[82:85], v[18:21], a[160:175]
	v_pk_mul_f16 v33, v139, v49
	s_nop 0
	v_pk_max_f16 v32, v32, v33
	s_nop 0
	v_cndmask_b32_e64 v33, v138, v32, s[16:17]
	v_cndmask_b32_e64 v32, v138, v32, s[18:19]
	v_mfma_f32_32x32x16_f16 a[128:143], v[10:13], v[18:21], a[128:143]
	v_perm_b32 v18, v1, v42, s20
	v_perm_b32 v19, v38, v39, s20
	v_perm_b32 v20, v30, v31, s20
	v_perm_b32 v21, v32, v33, s20
	v_mfma_f32_32x32x16_f16 a[144:159], v[82:85], v[6:9], a[144:159]
	v_pk_add_f16 v1, v19, v18
	v_pk_add_f16 v30, v20, v21
	s_nop 0
	v_pk_add_f16 v1, v1, v30
	s_nop 0
	v_dot2c_f32_f16_e32 v135, 0x3c003c00, v1
	v_mfma_f32_32x32x16_f16 a[80:95], v[10:13], v[6:9], a[80:95]
	s_waitcnt lgkmcnt(7)
	v_mfma_f32_32x32x16_f16 a[96:111], v[74:77], v[2:5], a[96:111]
	v_mfma_f32_32x32x16_f16 a[0:15], v[18:21], v[2:5], a[0:15]
	s_waitcnt lgkmcnt(6)
	v_mfma_f32_32x32x16_f16 a[240:255], v[74:77], v[14:17], a[240:255]
	v_mfma_f32_32x32x16_f16 a[16:31], v[18:21], v[14:17], a[16:31]
	s_waitcnt lgkmcnt(5)
	v_mfma_f32_32x32x16_f16 a[224:239], v[74:77], v[22:25], a[224:239]
	v_mfma_f32_32x32x16_f16 a[32:47], v[18:21], v[22:25], a[32:47]
	s_waitcnt lgkmcnt(4)
	v_mfma_f32_32x32x16_f16 a[208:223], v[74:77], v[26:29], a[208:223]
	v_mfma_f32_32x32x16_f16 a[48:63], v[18:21], v[26:29], a[48:63]
	s_waitcnt lgkmcnt(3)
	v_mfma_f32_32x32x16_f16 a[192:207], v[74:77], v[34:37], a[192:207]
	v_mfma_f32_32x32x16_f16 a[64:79], v[18:21], v[34:37], a[64:79]
	s_waitcnt lgkmcnt(2)
	v_mfma_f32_32x32x16_f16 a[176:191], v[74:77], v[50:53], a[176:191]
	v_mfma_f32_32x32x16_f16 a[112:127], v[18:21], v[50:53], a[112:127]
	s_waitcnt lgkmcnt(1)
	v_mfma_f32_32x32x16_f16 a[160:175], v[74:77], v[54:57], a[160:175]
	v_mfma_f32_32x32x16_f16 a[128:143], v[18:21], v[54:57], a[128:143]
	s_waitcnt lgkmcnt(0)
	v_mfma_f32_32x32x16_f16 a[144:159], v[74:77], v[58:61], a[144:159]
	v_mfma_f32_32x32x16_f16 a[80:95], v[18:21], v[58:61], a[80:95]
	v_readfirstlane_b32 s1, v0
	s_and_b32 s0, s3, 0xffffff00
	s_andn2_b32 s1, s1, 63
	s_add_i32 s4, s1, s0
	s_lshl_b32 s0, s2, 13
	s_and_b32 s6, s0, 0xe000
	s_ashr_i32 s5, s4, 31
	s_add_u32 s0, s4, s6
	s_addc_u32 s1, s5, 0
	s_lshl_b64 s[2:3], s[0:1], 9
	v_lshrrev_b32_e32 v0, 3, v132
	s_add_u32 s2, s22, s2
	v_and_b32_e32 v3, 12, v0
	s_addc_u32 s3, s23, s3
	v_lshlrev_b32_e32 v0, 9, v3
	v_mov_b32_e32 v1, 0
	v_lshl_add_u64 v[4:5], s[2:3], 0, v[0:1]
	v_lshlrev_b32_e32 v0, 4, v132
	v_and_b32_e32 v0, 0x1f0, v0
	v_lshl_add_u64 v[4:5], v[4:5], 0, v[0:1]
	v_accvgpr_read_b32 v6, a96
	v_accvgpr_read_b32 v7, a240
	v_accvgpr_read_b32 v8, a224
	v_max3_f32 v0, |v6|, |v7|, |v8|
	v_accvgpr_read_b32 v9, a208
	v_accvgpr_read_b32 v14, a192
	v_max3_f32 v0, |v0|, |v9|, |v14|
	v_accvgpr_read_b32 v15, a176
	v_accvgpr_read_b32 v16, a160
	v_max3_f32 v0, |v0|, |v15|, |v16|
	v_accvgpr_read_b32 v10, a144
	v_accvgpr_read_b32 v17, a144
	v_max3_f32 v10, |v0|, |v17|, |v10|
	v_accvgpr_read_b32 v18, a97
	v_accvgpr_read_b32 v19, a241
	v_accvgpr_read_b32 v20, a225
	v_max3_f32 v0, |v18|, |v19|, |v20|
	v_accvgpr_read_b32 v21, a209
	v_accvgpr_read_b32 v22, a193
	v_max3_f32 v0, |v0|, |v21|, |v22|
	v_accvgpr_read_b32 v23, a177
	v_accvgpr_read_b32 v24, a161
	v_max3_f32 v0, |v0|, |v23|, |v24|
	v_accvgpr_read_b32 v11, a145
	v_accvgpr_read_b32 v25, a145
	v_max3_f32 v11, |v0|, |v25|, |v11|
	v_accvgpr_read_b32 v26, a98
	v_accvgpr_read_b32 v27, a242
	v_accvgpr_read_b32 v28, a226
	v_max3_f32 v0, |v26|, |v27|, |v28|
	v_accvgpr_read_b32 v29, a210
	v_accvgpr_read_b32 v30, a194
	v_max3_f32 v0, |v0|, |v29|, |v30|
	v_accvgpr_read_b32 v31, a178
	v_accvgpr_read_b32 v32, a162
	v_max3_f32 v0, |v0|, |v31|, |v32|
	v_accvgpr_read_b32 v12, a146
	v_accvgpr_read_b32 v33, a146
	v_max3_f32 v12, |v0|, |v33|, |v12|
	v_accvgpr_read_b32 v34, a99
	v_accvgpr_read_b32 v35, a243
	v_accvgpr_read_b32 v36, a227
	v_max3_f32 v0, |v34|, |v35|, |v36|
	v_accvgpr_read_b32 v37, a211
	v_accvgpr_read_b32 v38, a195
	v_max3_f32 v0, |v0|, |v37|, |v38|
	v_accvgpr_read_b32 v13, a147
	v_accvgpr_read_b32 v39, a179
	v_accvgpr_read_b32 v40, a163
	v_max3_f32 v0, |v0|, |v39|, |v40|
	v_accvgpr_read_b32 v41, a147
	v_max3_f32 v13, |v0|, |v41|, |v13|
	v_lshlrev_b32_e32 v0, 2, v3
	s_nop 1
	v_max_f32_dpp v10, v10, v10 quad_perm:[1,0,3,2] row_mask:0xf bank_mask:0xf
	v_max_f32_dpp v11, v11, v11 quad_perm:[1,0,3,2] row_mask:0xf bank_mask:0xf
	v_max_f32_dpp v12, v12, v12 quad_perm:[1,0,3,2] row_mask:0xf bank_mask:0xf
	v_max_f32_dpp v13, v13, v13 quad_perm:[1,0,3,2] row_mask:0xf bank_mask:0xf
	v_max_f32_dpp v10, v10, v10 quad_perm:[2,3,0,1] row_mask:0xf bank_mask:0xf
	v_max_f32_dpp v11, v11, v11 quad_perm:[2,3,0,1] row_mask:0xf bank_mask:0xf
	v_max_f32_dpp v12, v12, v12 quad_perm:[2,3,0,1] row_mask:0xf bank_mask:0xf
	v_max_f32_dpp v13, v13, v13 quad_perm:[2,3,0,1] row_mask:0xf bank_mask:0xf
	v_max_f32_dpp v10, v10, v10 row_half_mirror row_mask:0xf bank_mask:0xf
	v_max_f32_dpp v11, v11, v11 row_half_mirror row_mask:0xf bank_mask:0xf
	v_max_f32_dpp v12, v12, v12 row_half_mirror row_mask:0xf bank_mask:0xf
	v_max_f32_dpp v13, v13, v13 row_half_mirror row_mask:0xf bank_mask:0xf
	v_max_f32_dpp v10, v10, v10 row_mirror row_mask:0xf bank_mask:0xf
	v_max_f32_dpp v11, v11, v11 row_mirror row_mask:0xf bank_mask:0xf
	v_max_f32_dpp v12, v12, v12 row_mirror row_mask:0xf bank_mask:0xf
	v_max_f32_dpp v13, v13, v13 row_mirror row_mask:0xf bank_mask:0xf
	s_nop 0
	ds_swizzle_b32 v42, v10 offset:swizzle(SWAP,16)
	s_waitcnt lgkmcnt(0)
	v_max_f32_e32 v10, v10, v42
	ds_swizzle_b32 v3, v12 offset:swizzle(SWAP,16)
	v_rcp_f32_e32 v42, v10
	v_cmp_lt_f32_e32 vcc, 0, v10
	s_waitcnt lgkmcnt(0)
	v_max_f32_e32 v12, v12, v3
	ds_swizzle_b32 v43, v11 offset:swizzle(SWAP,16)
	s_waitcnt lgkmcnt(0)
	v_max_f32_e32 v11, v11, v43
	s_lshl_b32 s2, s6, 2
	v_cndmask_b32_e32 v3, 0, v42, vcc
	v_pk_mul_f32 v[224:225], v[6:7], v[2:3] op_sel:[0,1] op_sel_hi:[1,1]
	v_pk_mul_f32 v[226:227], v[8:9], v[2:3] op_sel:[0,1] op_sel_hi:[1,1]
	v_cvt_pknorm_i16_f32 v6, v224, v225
	v_cvt_pknorm_i16_f32 v7, v226, v227
	v_pk_mul_f32 v[228:229], v[14:15], v[2:3] op_sel:[0,1] op_sel_hi:[1,1]
	v_rcp_f32_e32 v14, v11
	v_cvt_pknorm_i16_f32 v8, v228, v229
	v_pk_mul_f32 v[230:231], v[16:17], v[2:3] op_sel:[0,1] op_sel_hi:[1,1]
	v_cmp_lt_f32_e32 vcc, 0, v11
	v_cvt_pknorm_i16_f32 v9, v230, v231
	global_store_dwordx4 v[4:5], v[6:9], off sc0 sc1
	s_nop 1
	s_add_u32 s6, s24, s2
	v_cndmask_b32_e32 v3, 0, v14, vcc
	v_pk_mul_f32 v[224:225], v[18:19], v[2:3] op_sel:[0,1] op_sel_hi:[1,1]
	v_pk_mul_f32 v[226:227], v[20:21], v[2:3] op_sel:[0,1] op_sel_hi:[1,1]
	v_cvt_pknorm_i16_f32 v6, v224, v225
	v_cvt_pknorm_i16_f32 v7, v226, v227
	v_pk_mul_f32 v[228:229], v[22:23], v[2:3] op_sel:[0,1] op_sel_hi:[1,1]
	v_pk_mul_f32 v[230:231], v[24:25], v[2:3] op_sel:[0,1] op_sel_hi:[1,1]
	v_cvt_pknorm_i16_f32 v8, v228, v229
	v_cvt_pknorm_i16_f32 v9, v230, v231
	v_rcp_f32_e32 v3, v12
	s_addc_u32 s7, s25, 0
	s_lshl_b64 s[2:3], s[4:5], 2
	s_mov_b64 s[4:5], 0x200
	s_add_u32 s2, s6, s2
	v_lshl_add_u64 v[14:15], v[4:5], 0, s[4:5]
	s_mov_b32 s4, 0x38000100
	v_cmp_lt_f32_e32 vcc, 0, v12
	s_addc_u32 s3, s7, s3
	global_store_dwordx4 v[14:15], v[6:9], off sc0 sc1
	s_nop 1
	v_pk_mul_f32 v[6:7], v[10:11], s[4:5] op_sel_hi:[1,0]
	v_cndmask_b32_e32 v3, 0, v3, vcc
	global_store_dwordx2 v0, v[6:7], s[2:3]
	v_pk_mul_f32 v[224:225], v[26:27], v[2:3] op_sel:[0,1] op_sel_hi:[1,1]
	v_pk_mul_f32 v[226:227], v[28:29], v[2:3] op_sel:[0,1] op_sel_hi:[1,1]
	v_cvt_pknorm_i16_f32 v6, v224, v225
	v_cvt_pknorm_i16_f32 v7, v226, v227
	v_pk_mul_f32 v[228:229], v[30:31], v[2:3] op_sel:[0,1] op_sel_hi:[1,1]
	v_pk_mul_f32 v[230:231], v[32:33], v[2:3] op_sel:[0,1] op_sel_hi:[1,1]
	v_cvt_pknorm_i16_f32 v8, v228, v229
	ds_swizzle_b32 v44, v13 offset:swizzle(SWAP,16)
	s_waitcnt lgkmcnt(0)
	v_max_f32_e32 v13, v13, v44
	v_cvt_pknorm_i16_f32 v9, v230, v231
	v_rcp_f32_e32 v3, v13
	v_cmp_lt_f32_e32 vcc, 0, v13
	s_mov_b64 s[6:7], 0x400
	v_lshl_add_u64 v[10:11], v[4:5], 0, s[6:7]
	v_cndmask_b32_e32 v3, 0, v3, vcc
	global_store_dwordx4 v[10:11], v[6:9], off sc0 sc1
	s_nop 1
	v_pk_mul_f32 v[224:225], v[34:35], v[2:3] op_sel:[0,1] op_sel_hi:[1,1]
	v_pk_mul_f32 v[226:227], v[36:37], v[2:3] op_sel:[0,1] op_sel_hi:[1,1]
	v_cvt_pknorm_i16_f32 v6, v224, v225
	v_cvt_pknorm_i16_f32 v7, v226, v227
	v_pk_mul_f32 v[228:229], v[38:39], v[2:3] op_sel:[0,1] op_sel_hi:[1,1]
	v_pk_mul_f32 v[230:231], v[40:41], v[2:3] op_sel:[0,1] op_sel_hi:[1,1]
	v_cvt_pknorm_i16_f32 v8, v228, v229
	s_mov_b64 s[6:7], 0x600
	v_cvt_pknorm_i16_f32 v9, v230, v231
	v_lshl_add_u64 v[10:11], v[4:5], 0, s[6:7]
	global_store_dwordx4 v[10:11], v[6:9], off sc0 sc1
	s_nop 1
	v_pk_mul_f32 v[6:7], v[12:13], s[4:5] op_sel_hi:[1,0]
	v_lshlrev_b32_e32 v2, 2, v132
	global_store_dwordx2 v0, v[6:7], s[2:3] offset:8
	v_accvgpr_read_b32 v42, a100
	v_accvgpr_read_b32 v6, a244
	v_accvgpr_read_b32 v7, a228
	v_max3_f32 v8, |v42|, |v6|, |v7|
	v_accvgpr_read_b32 v9, a212
	v_accvgpr_read_b32 v14, a196
	v_max3_f32 v8, |v8|, |v9|, |v14|
	v_accvgpr_read_b32 v15, a180
	v_accvgpr_read_b32 v16, a164
	v_max3_f32 v8, |v8|, |v15|, |v16|
	v_accvgpr_read_b32 v10, a148
	v_accvgpr_read_b32 v43, a101
	v_accvgpr_read_b32 v17, a148
	v_max3_f32 v8, |v8|, |v17|, |v10|
	v_accvgpr_read_b32 v19, a245
	v_accvgpr_read_b32 v20, a229
	v_max3_f32 v10, |v43|, |v19|, |v20|
	v_accvgpr_read_b32 v21, a213
	v_accvgpr_read_b32 v22, a197
	v_max3_f32 v10, |v10|, |v21|, |v22|
	v_accvgpr_read_b32 v23, a181
	v_accvgpr_read_b32 v24, a165
	v_max3_f32 v10, |v10|, |v23|, |v24|
	v_accvgpr_read_b32 v11, a149
	v_accvgpr_read_b32 v44, a102
	v_accvgpr_read_b32 v25, a149
	v_max3_f32 v11, |v10|, |v25|, |v11|
	v_accvgpr_read_b32 v27, a246
	v_accvgpr_read_b32 v28, a230
	v_max3_f32 v10, |v44|, |v27|, |v28|
	v_accvgpr_read_b32 v29, a214
	v_accvgpr_read_b32 v30, a198
	v_max3_f32 v10, |v10|, |v29|, |v30|
	v_accvgpr_read_b32 v31, a182
	v_accvgpr_read_b32 v32, a166
	v_max3_f32 v10, |v10|, |v31|, |v32|
	v_accvgpr_read_b32 v12, a150
	v_accvgpr_read_b32 v45, a103
	v_accvgpr_read_b32 v33, a150
	v_max3_f32 v12, |v10|, |v33|, |v12|
	v_accvgpr_read_b32 v35, a247
	v_accvgpr_read_b32 v36, a231
	v_max3_f32 v10, |v45|, |v35|, |v36|
	v_accvgpr_read_b32 v37, a215
	v_accvgpr_read_b32 v38, a199
	v_max3_f32 v10, |v10|, |v37|, |v38|
	v_accvgpr_read_b32 v13, a151
	v_accvgpr_read_b32 v39, a183
	v_accvgpr_read_b32 v40, a167
	v_max3_f32 v10, |v10|, |v39|, |v40|
	v_accvgpr_read_b32 v41, a151
	v_max3_f32 v13, |v10|, |v41|, |v13|
	v_mov_b32_e32 v3, v42
	s_nop 1
	v_max_f32_dpp v8, v8, v8 quad_perm:[1,0,3,2] row_mask:0xf bank_mask:0xf
	v_max_f32_dpp v11, v11, v11 quad_perm:[1,0,3,2] row_mask:0xf bank_mask:0xf
	v_max_f32_dpp v12, v12, v12 quad_perm:[1,0,3,2] row_mask:0xf bank_mask:0xf
	v_max_f32_dpp v13, v13, v13 quad_perm:[1,0,3,2] row_mask:0xf bank_mask:0xf
	v_max_f32_dpp v8, v8, v8 quad_perm:[2,3,0,1] row_mask:0xf bank_mask:0xf
	v_max_f32_dpp v11, v11, v11 quad_perm:[2,3,0,1] row_mask:0xf bank_mask:0xf
	v_max_f32_dpp v12, v12, v12 quad_perm:[2,3,0,1] row_mask:0xf bank_mask:0xf
	v_max_f32_dpp v13, v13, v13 quad_perm:[2,3,0,1] row_mask:0xf bank_mask:0xf
	v_max_f32_dpp v8, v8, v8 row_half_mirror row_mask:0xf bank_mask:0xf
	v_max_f32_dpp v11, v11, v11 row_half_mirror row_mask:0xf bank_mask:0xf
	v_max_f32_dpp v12, v12, v12 row_half_mirror row_mask:0xf bank_mask:0xf
	v_max_f32_dpp v13, v13, v13 row_half_mirror row_mask:0xf bank_mask:0xf
	v_max_f32_dpp v8, v8, v8 row_mirror row_mask:0xf bank_mask:0xf
	v_max_f32_dpp v11, v11, v11 row_mirror row_mask:0xf bank_mask:0xf
	v_max_f32_dpp v12, v12, v12 row_mirror row_mask:0xf bank_mask:0xf
	v_max_f32_dpp v13, v13, v13 row_mirror row_mask:0xf bank_mask:0xf
	s_nop 0
	ds_swizzle_b32 v10, v8 offset:swizzle(SWAP,16)
	s_waitcnt lgkmcnt(0)
	v_max_f32_e32 v10, v8, v10
	ds_swizzle_b32 v42, v11 offset:swizzle(SWAP,16)
	v_rcp_f32_e32 v8, v10
	v_cmp_lt_f32_e32 vcc, 0, v10
	s_waitcnt lgkmcnt(0)
	v_max_f32_e32 v11, v11, v42
	v_mov_b32_e32 v18, v43
	s_mov_b64 s[6:7], 0x1000
	v_cndmask_b32_e32 v42, 0, v8, vcc
	v_mul_f32_e32 v3, v42, v3
	v_mul_f32_e32 v6, v42, v6
	v_cvt_pknorm_i16_f32 v6, v3, v6
	v_mul_f32_e32 v3, v42, v7
	v_mul_f32_e32 v7, v42, v9
	v_cvt_pknorm_i16_f32 v7, v3, v7
	v_pk_mul_f32 v[224:225], v[14:15], v[42:43] op_sel_hi:[1,0]
	v_pk_mul_f32 v[226:227], v[16:17], v[42:43] op_sel_hi:[1,0]
	v_cvt_pknorm_i16_f32 v8, v224, v225
	v_cvt_pknorm_i16_f32 v9, v226, v227
	v_rcp_f32_e32 v3, v11
	v_cmp_lt_f32_e32 vcc, 0, v11
	v_lshl_add_u64 v[14:15], v[4:5], 0, s[6:7]
	global_store_dwordx4 v[14:15], v[6:9], off sc0 sc1
	s_nop 1
	ds_swizzle_b32 v43, v12 offset:swizzle(SWAP,16)
	v_cndmask_b32_e32 v3, 0, v3, vcc
	v_pk_mul_f32 v[228:229], v[18:19], v[2:3] op_sel:[0,1] op_sel_hi:[1,1]
	v_pk_mul_f32 v[230:231], v[20:21], v[2:3] op_sel:[0,1] op_sel_hi:[1,1]
	v_cvt_pknorm_i16_f32 v6, v228, v229
	v_cvt_pknorm_i16_f32 v7, v230, v231
	v_pk_mul_f32 v[224:225], v[22:23], v[2:3] op_sel:[0,1] op_sel_hi:[1,1]
	v_pk_mul_f32 v[226:227], v[24:25], v[2:3] op_sel:[0,1] op_sel_hi:[1,1]
	v_cvt_pknorm_i16_f32 v8, v224, v225
	s_waitcnt lgkmcnt(0)
	v_max_f32_e32 v12, v12, v43
	v_cvt_pknorm_i16_f32 v9, v226, v227
	v_rcp_f32_e32 v3, v12
	s_mov_b64 s[6:7], 0x1200
	v_cmp_lt_f32_e32 vcc, 0, v12
	v_mov_b32_e32 v26, v44
	v_lshl_add_u64 v[14:15], v[4:5], 0, s[6:7]
	global_store_dwordx4 v[14:15], v[6:9], off sc0 sc1
	s_nop 1
	v_pk_mul_f32 v[6:7], v[10:11], s[4:5] op_sel_hi:[1,0]
	v_cndmask_b32_e32 v3, 0, v3, vcc
	global_store_dwordx2 v0, v[6:7], s[2:3] offset:32
	v_pk_mul_f32 v[228:229], v[26:27], v[2:3] op_sel:[0,1] op_sel_hi:[1,1]
	v_pk_mul_f32 v[230:231], v[28:29], v[2:3] op_sel:[0,1] op_sel_hi:[1,1]
	v_cvt_pknorm_i16_f32 v6, v228, v229
	v_cvt_pknorm_i16_f32 v7, v230, v231
	v_pk_mul_f32 v[224:225], v[30:31], v[2:3] op_sel:[0,1] op_sel_hi:[1,1]
	v_pk_mul_f32 v[226:227], v[32:33], v[2:3] op_sel:[0,1] op_sel_hi:[1,1]
	v_cvt_pknorm_i16_f32 v8, v224, v225
	ds_swizzle_b32 v44, v13 offset:swizzle(SWAP,16)
	s_waitcnt lgkmcnt(0)
	v_max_f32_e32 v13, v13, v44
	v_cvt_pknorm_i16_f32 v9, v226, v227
	v_rcp_f32_e32 v3, v13
	v_cmp_lt_f32_e32 vcc, 0, v13
	v_mov_b32_e32 v34, v45
	s_mov_b64 s[6:7], 0x1400
	v_cndmask_b32_e32 v3, 0, v3, vcc
	v_lshl_add_u64 v[10:11], v[4:5], 0, s[6:7]
	global_store_dwordx4 v[10:11], v[6:9], off sc0 sc1
	s_nop 1
	v_pk_mul_f32 v[228:229], v[34:35], v[2:3] op_sel:[0,1] op_sel_hi:[1,1]
	v_pk_mul_f32 v[230:231], v[36:37], v[2:3] op_sel:[0,1] op_sel_hi:[1,1]
	v_cvt_pknorm_i16_f32 v6, v228, v229
	v_cvt_pknorm_i16_f32 v7, v230, v231
	v_pk_mul_f32 v[224:225], v[38:39], v[2:3] op_sel:[0,1] op_sel_hi:[1,1]
	v_pk_mul_f32 v[226:227], v[40:41], v[2:3] op_sel:[0,1] op_sel_hi:[1,1]
	v_cvt_pknorm_i16_f32 v8, v224, v225
	s_mov_b64 s[6:7], 0x1600
	v_cvt_pknorm_i16_f32 v9, v226, v227
	v_lshl_add_u64 v[10:11], v[4:5], 0, s[6:7]
	global_store_dwordx4 v[10:11], v[6:9], off sc0 sc1
	s_nop 1
	v_pk_mul_f32 v[6:7], v[12:13], s[4:5] op_sel_hi:[1,0]
	v_accvgpr_read_b32 v46, a104
	v_accvgpr_read_b32 v47, a105
	v_accvgpr_read_b32 v48, a106
	v_accvgpr_read_b32 v49, a107
	v_accvgpr_read_b32 v50, a108
	v_accvgpr_read_b32 v51, a109
	v_accvgpr_read_b32 v52, a110
	v_accvgpr_read_b32 v53, a111
	global_store_dwordx2 v0, v[6:7], s[2:3] offset:40
	v_mov_b64_e32 v[42:43], v[46:47]
	v_accvgpr_read_b32 v6, a248
	v_accvgpr_read_b32 v7, a232
	v_max3_f32 v8, |v42|, |v6|, |v7|
	v_accvgpr_read_b32 v9, a216
	v_accvgpr_read_b32 v14, a200
	v_max3_f32 v8, |v8|, |v9|, |v14|
	v_accvgpr_read_b32 v15, a184
	v_accvgpr_read_b32 v16, a168
	v_max3_f32 v8, |v8|, |v15|, |v16|
	v_accvgpr_read_b32 v10, a152
	v_accvgpr_read_b32 v17, a152
	v_max3_f32 v8, |v8|, |v17|, |v10|
	v_accvgpr_read_b32 v19, a249
	v_accvgpr_read_b32 v20, a233
	v_max3_f32 v10, |v43|, |v19|, |v20|
	v_accvgpr_read_b32 v21, a217
	v_accvgpr_read_b32 v22, a201
	v_max3_f32 v10, |v10|, |v21|, |v22|
	v_accvgpr_read_b32 v23, a185
	v_accvgpr_read_b32 v24, a169
	v_max3_f32 v10, |v10|, |v23|, |v24|
	v_accvgpr_read_b32 v11, a153
	v_mov_b64_e32 v[44:45], v[48:49]
	v_accvgpr_read_b32 v25, a153
	v_max3_f32 v11, |v10|, |v25|, |v11|
	v_accvgpr_read_b32 v27, a250
	v_accvgpr_read_b32 v28, a234
	v_max3_f32 v10, |v44|, |v27|, |v28|
	v_accvgpr_read_b32 v29, a218
	v_accvgpr_read_b32 v30, a202
	v_max3_f32 v10, |v10|, |v29|, |v30|
	v_accvgpr_read_b32 v31, a186
	v_accvgpr_read_b32 v32, a170
	v_max3_f32 v10, |v10|, |v31|, |v32|
	v_accvgpr_read_b32 v12, a154
	v_accvgpr_read_b32 v33, a154
	v_max3_f32 v12, |v10|, |v33|, |v12|
	v_accvgpr_read_b32 v35, a251
	v_accvgpr_read_b32 v36, a235
	v_max3_f32 v10, |v45|, |v35|, |v36|
	v_accvgpr_read_b32 v37, a219
	v_accvgpr_read_b32 v38, a203
	v_max3_f32 v10, |v10|, |v37|, |v38|
	v_accvgpr_read_b32 v13, a155
	v_accvgpr_read_b32 v39, a187
	v_accvgpr_read_b32 v40, a171
	v_max3_f32 v10, |v10|, |v39|, |v40|
	v_accvgpr_read_b32 v41, a155
	v_max3_f32 v13, |v10|, |v41|, |v13|
	v_mov_b32_e32 v3, v42
	s_nop 1
	v_max_f32_dpp v8, v8, v8 quad_perm:[1,0,3,2] row_mask:0xf bank_mask:0xf
	v_max_f32_dpp v11, v11, v11 quad_perm:[1,0,3,2] row_mask:0xf bank_mask:0xf
	v_max_f32_dpp v12, v12, v12 quad_perm:[1,0,3,2] row_mask:0xf bank_mask:0xf
	v_max_f32_dpp v13, v13, v13 quad_perm:[1,0,3,2] row_mask:0xf bank_mask:0xf
	v_max_f32_dpp v8, v8, v8 quad_perm:[2,3,0,1] row_mask:0xf bank_mask:0xf
	v_max_f32_dpp v11, v11, v11 quad_perm:[2,3,0,1] row_mask:0xf bank_mask:0xf
	v_max_f32_dpp v12, v12, v12 quad_perm:[2,3,0,1] row_mask:0xf bank_mask:0xf
	v_max_f32_dpp v13, v13, v13 quad_perm:[2,3,0,1] row_mask:0xf bank_mask:0xf
	v_max_f32_dpp v8, v8, v8 row_half_mirror row_mask:0xf bank_mask:0xf
	v_max_f32_dpp v11, v11, v11 row_half_mirror row_mask:0xf bank_mask:0xf
	v_max_f32_dpp v12, v12, v12 row_half_mirror row_mask:0xf bank_mask:0xf
	v_max_f32_dpp v13, v13, v13 row_half_mirror row_mask:0xf bank_mask:0xf
	v_max_f32_dpp v8, v8, v8 row_mirror row_mask:0xf bank_mask:0xf
	v_max_f32_dpp v11, v11, v11 row_mirror row_mask:0xf bank_mask:0xf
	v_max_f32_dpp v12, v12, v12 row_mirror row_mask:0xf bank_mask:0xf
	v_max_f32_dpp v13, v13, v13 row_mirror row_mask:0xf bank_mask:0xf
	s_nop 0
	ds_swizzle_b32 v10, v8 offset:swizzle(SWAP,16)
	s_waitcnt lgkmcnt(0)
	v_max_f32_e32 v10, v8, v10
	ds_swizzle_b32 v42, v11 offset:swizzle(SWAP,16)
	v_rcp_f32_e32 v8, v10
	v_cmp_lt_f32_e32 vcc, 0, v10
	s_waitcnt lgkmcnt(0)
	v_max_f32_e32 v11, v11, v42
	v_mov_b32_e32 v18, v43
	s_mov_b64 s[6:7], 0x2000
	v_cndmask_b32_e32 v42, 0, v8, vcc
	v_mul_f32_e32 v3, v42, v3
	v_mul_f32_e32 v6, v42, v6
	v_cvt_pknorm_i16_f32 v6, v3, v6
	v_mul_f32_e32 v3, v42, v7
	v_mul_f32_e32 v7, v42, v9
	v_cvt_pknorm_i16_f32 v7, v3, v7
	v_pk_mul_f32 v[228:229], v[14:15], v[42:43] op_sel_hi:[1,0]
	v_pk_mul_f32 v[230:231], v[16:17], v[42:43] op_sel_hi:[1,0]
	v_cvt_pknorm_i16_f32 v8, v228, v229
	v_cvt_pknorm_i16_f32 v9, v230, v231
	v_rcp_f32_e32 v3, v11
	v_cmp_lt_f32_e32 vcc, 0, v11
	v_lshl_add_u64 v[14:15], v[4:5], 0, s[6:7]
	global_store_dwordx4 v[14:15], v[6:9], off sc0 sc1
	s_nop 1
	ds_swizzle_b32 v43, v12 offset:swizzle(SWAP,16)
	v_cndmask_b32_e32 v3, 0, v3, vcc
	v_pk_mul_f32 v[224:225], v[18:19], v[2:3] op_sel:[0,1] op_sel_hi:[1,1]
	v_pk_mul_f32 v[226:227], v[20:21], v[2:3] op_sel:[0,1] op_sel_hi:[1,1]
	v_cvt_pknorm_i16_f32 v6, v224, v225
	v_cvt_pknorm_i16_f32 v7, v226, v227
	v_pk_mul_f32 v[228:229], v[22:23], v[2:3] op_sel:[0,1] op_sel_hi:[1,1]
	v_pk_mul_f32 v[230:231], v[24:25], v[2:3] op_sel:[0,1] op_sel_hi:[1,1]
	v_cvt_pknorm_i16_f32 v8, v228, v229
	s_waitcnt lgkmcnt(0)
	v_max_f32_e32 v12, v12, v43
	v_cvt_pknorm_i16_f32 v9, v230, v231
	v_rcp_f32_e32 v3, v12
	s_mov_b64 s[6:7], 0x2200
	v_cmp_lt_f32_e32 vcc, 0, v12
	v_mov_b32_e32 v26, v44
	v_lshl_add_u64 v[14:15], v[4:5], 0, s[6:7]
	global_store_dwordx4 v[14:15], v[6:9], off sc0 sc1
	s_nop 1
	v_pk_mul_f32 v[6:7], v[10:11], s[4:5] op_sel_hi:[1,0]
	v_cndmask_b32_e32 v3, 0, v3, vcc
	global_store_dwordx2 v0, v[6:7], s[2:3] offset:64
	v_pk_mul_f32 v[224:225], v[26:27], v[2:3] op_sel:[0,1] op_sel_hi:[1,1]
	v_pk_mul_f32 v[226:227], v[28:29], v[2:3] op_sel:[0,1] op_sel_hi:[1,1]
	v_cvt_pknorm_i16_f32 v6, v224, v225
	v_cvt_pknorm_i16_f32 v7, v226, v227
	v_pk_mul_f32 v[228:229], v[30:31], v[2:3] op_sel:[0,1] op_sel_hi:[1,1]
	v_pk_mul_f32 v[230:231], v[32:33], v[2:3] op_sel:[0,1] op_sel_hi:[1,1]
	v_cvt_pknorm_i16_f32 v8, v228, v229
	ds_swizzle_b32 v44, v13 offset:swizzle(SWAP,16)
	s_waitcnt lgkmcnt(0)
	v_max_f32_e32 v13, v13, v44
	v_cvt_pknorm_i16_f32 v9, v230, v231
	v_rcp_f32_e32 v3, v13
	v_cmp_lt_f32_e32 vcc, 0, v13
	v_mov_b32_e32 v34, v45
	s_mov_b64 s[6:7], 0x2400
	v_cndmask_b32_e32 v3, 0, v3, vcc
	v_lshl_add_u64 v[10:11], v[4:5], 0, s[6:7]
	global_store_dwordx4 v[10:11], v[6:9], off sc0 sc1
	s_nop 1
	v_pk_mul_f32 v[224:225], v[34:35], v[2:3] op_sel:[0,1] op_sel_hi:[1,1]
	v_pk_mul_f32 v[226:227], v[36:37], v[2:3] op_sel:[0,1] op_sel_hi:[1,1]
	v_cvt_pknorm_i16_f32 v6, v224, v225
	v_cvt_pknorm_i16_f32 v7, v226, v227
	v_pk_mul_f32 v[228:229], v[38:39], v[2:3] op_sel:[0,1] op_sel_hi:[1,1]
	v_pk_mul_f32 v[230:231], v[40:41], v[2:3] op_sel:[0,1] op_sel_hi:[1,1]
	v_cvt_pknorm_i16_f32 v8, v228, v229
	s_mov_b64 s[6:7], 0x2600
	v_cvt_pknorm_i16_f32 v9, v230, v231
	v_lshl_add_u64 v[10:11], v[4:5], 0, s[6:7]
	global_store_dwordx4 v[10:11], v[6:9], off sc0 sc1
	s_nop 1
	v_pk_mul_f32 v[6:7], v[12:13], s[4:5] op_sel_hi:[1,0]
	v_mov_b64_e32 v[46:47], v[50:51]
	v_mov_b64_e32 v[48:49], v[52:53]
	global_store_dwordx2 v0, v[6:7], s[2:3] offset:72
	v_mov_b64_e32 v[32:33], v[46:47]
	v_accvgpr_read_b32 v6, a252
	v_accvgpr_read_b32 v7, a236
	v_max3_f32 v8, |v32|, |v6|, |v7|
	v_accvgpr_read_b32 v9, a220
	v_accvgpr_read_b32 v14, a204
	v_max3_f32 v8, |v8|, |v9|, |v14|
	v_accvgpr_read_b32 v15, a188
	v_accvgpr_read_b32 v16, a172
	v_max3_f32 v8, |v8|, |v15|, |v16|
	v_accvgpr_read_b32 v10, a156
	v_accvgpr_read_b32 v17, a156
	v_max3_f32 v8, |v8|, |v17|, |v10|
	v_accvgpr_read_b32 v19, a253
	v_accvgpr_read_b32 v20, a237
	v_max3_f32 v10, |v33|, |v19|, |v20|
	v_accvgpr_read_b32 v21, a221
	v_accvgpr_read_b32 v22, a205
	v_max3_f32 v10, |v10|, |v21|, |v22|
	v_accvgpr_read_b32 v23, a189
	v_accvgpr_read_b32 v24, a173
	v_max3_f32 v10, |v10|, |v23|, |v24|
	v_accvgpr_read_b32 v11, a157
	v_mov_b64_e32 v[34:35], v[48:49]
	v_accvgpr_read_b32 v25, a157
	v_max3_f32 v11, |v10|, |v25|, |v11|
	v_accvgpr_read_b32 v27, a254
	v_accvgpr_read_b32 v28, a238
	v_max3_f32 v10, |v34|, |v27|, |v28|
	v_accvgpr_read_b32 v29, a222
	v_accvgpr_read_b32 v30, a206
	v_max3_f32 v10, |v10|, |v29|, |v30|
	v_mov_b32_e32 v3, v32
	v_accvgpr_read_b32 v31, a190
	v_accvgpr_read_b32 v32, a174
	v_max3_f32 v10, |v10|, |v31|, |v32|
	v_accvgpr_read_b32 v12, a158
	v_mov_b32_e32 v18, v33
	v_mov_b32_e32 v26, v34
	v_accvgpr_read_b32 v33, a158
	v_max3_f32 v12, |v10|, |v33|, |v12|
	v_mov_b32_e32 v34, v35
	v_accvgpr_read_b32 v35, a255
	v_accvgpr_read_b32 v36, a239
	v_max3_f32 v10, |v34|, |v35|, |v36|
	v_accvgpr_read_b32 v37, a223
	v_accvgpr_read_b32 v38, a207
	v_max3_f32 v10, |v10|, |v37|, |v38|
	v_accvgpr_read_b32 v13, a159
	v_accvgpr_read_b32 v39, a191
	v_accvgpr_read_b32 v40, a175
	v_max3_f32 v10, |v10|, |v39|, |v40|
	v_accvgpr_read_b32 v41, a159
	v_max3_f32 v13, |v10|, |v41|, |v13|
	s_mov_b64 s[6:7], 0x3000
	s_nop 1
	v_max_f32_dpp v8, v8, v8 quad_perm:[1,0,3,2] row_mask:0xf bank_mask:0xf
	v_max_f32_dpp v11, v11, v11 quad_perm:[1,0,3,2] row_mask:0xf bank_mask:0xf
	v_max_f32_dpp v12, v12, v12 quad_perm:[1,0,3,2] row_mask:0xf bank_mask:0xf
	v_max_f32_dpp v13, v13, v13 quad_perm:[1,0,3,2] row_mask:0xf bank_mask:0xf
	v_max_f32_dpp v8, v8, v8 quad_perm:[2,3,0,1] row_mask:0xf bank_mask:0xf
	v_max_f32_dpp v11, v11, v11 quad_perm:[2,3,0,1] row_mask:0xf bank_mask:0xf
	v_max_f32_dpp v12, v12, v12 quad_perm:[2,3,0,1] row_mask:0xf bank_mask:0xf
	v_max_f32_dpp v13, v13, v13 quad_perm:[2,3,0,1] row_mask:0xf bank_mask:0xf
	v_max_f32_dpp v8, v8, v8 row_half_mirror row_mask:0xf bank_mask:0xf
	v_max_f32_dpp v11, v11, v11 row_half_mirror row_mask:0xf bank_mask:0xf
	v_max_f32_dpp v12, v12, v12 row_half_mirror row_mask:0xf bank_mask:0xf
	v_max_f32_dpp v13, v13, v13 row_half_mirror row_mask:0xf bank_mask:0xf
	v_max_f32_dpp v8, v8, v8 row_mirror row_mask:0xf bank_mask:0xf
	v_max_f32_dpp v11, v11, v11 row_mirror row_mask:0xf bank_mask:0xf
	v_max_f32_dpp v12, v12, v12 row_mirror row_mask:0xf bank_mask:0xf
	v_max_f32_dpp v13, v13, v13 row_mirror row_mask:0xf bank_mask:0xf
	s_nop 0
	ds_swizzle_b32 v10, v8 offset:swizzle(SWAP,16)
	s_waitcnt lgkmcnt(0)
	v_max_f32_e32 v10, v8, v10
	ds_swizzle_b32 v42, v11 offset:swizzle(SWAP,16)
	v_rcp_f32_e32 v8, v10
	v_cmp_lt_f32_e32 vcc, 0, v10
	s_waitcnt lgkmcnt(0)
	v_max_f32_e32 v11, v11, v42
	ds_swizzle_b32 v43, v12 offset:swizzle(SWAP,16)
	s_waitcnt lgkmcnt(0)
	v_max_f32_e32 v12, v12, v43
	ds_swizzle_b32 v44, v13 offset:swizzle(SWAP,16)
	v_cndmask_b32_e32 v42, 0, v8, vcc
	v_mul_f32_e32 v3, v42, v3
	v_mul_f32_e32 v6, v42, v6
	v_cvt_pknorm_i16_f32 v6, v3, v6
	v_mul_f32_e32 v3, v42, v7
	v_mul_f32_e32 v7, v42, v9
	v_cvt_pknorm_i16_f32 v7, v3, v7
	v_pk_mul_f32 v[224:225], v[14:15], v[42:43] op_sel_hi:[1,0]
	v_pk_mul_f32 v[226:227], v[16:17], v[42:43] op_sel_hi:[1,0]
	v_cvt_pknorm_i16_f32 v8, v224, v225
	v_cvt_pknorm_i16_f32 v9, v226, v227
	v_rcp_f32_e32 v3, v11
	v_cmp_lt_f32_e32 vcc, 0, v11
	v_lshl_add_u64 v[14:15], v[4:5], 0, s[6:7]
	global_store_dwordx4 v[14:15], v[6:9], off sc0 sc1
	s_nop 1
	s_mov_b64 s[6:7], 0x3200
	v_cndmask_b32_e32 v3, 0, v3, vcc
	v_pk_mul_f32 v[228:229], v[18:19], v[2:3] op_sel:[0,1] op_sel_hi:[1,1]
	v_pk_mul_f32 v[230:231], v[20:21], v[2:3] op_sel:[0,1] op_sel_hi:[1,1]
	v_cvt_pknorm_i16_f32 v6, v228, v229
	v_cvt_pknorm_i16_f32 v7, v230, v231
	v_pk_mul_f32 v[224:225], v[22:23], v[2:3] op_sel:[0,1] op_sel_hi:[1,1]
	v_pk_mul_f32 v[226:227], v[24:25], v[2:3] op_sel:[0,1] op_sel_hi:[1,1]
	v_cvt_pknorm_i16_f32 v8, v224, v225
	v_cvt_pknorm_i16_f32 v9, v226, v227
	v_rcp_f32_e32 v3, v12
	v_cmp_lt_f32_e32 vcc, 0, v12
	v_lshl_add_u64 v[14:15], v[4:5], 0, s[6:7]
	global_store_dwordx4 v[14:15], v[6:9], off sc0 sc1
	s_nop 1
	v_pk_mul_f32 v[6:7], v[10:11], s[4:5] op_sel_hi:[1,0]
	v_cndmask_b32_e32 v3, 0, v3, vcc
	global_store_dwordx2 v0, v[6:7], s[2:3] offset:96
	v_pk_mul_f32 v[228:229], v[26:27], v[2:3] op_sel:[0,1] op_sel_hi:[1,1]
	v_pk_mul_f32 v[230:231], v[28:29], v[2:3] op_sel:[0,1] op_sel_hi:[1,1]
	v_cvt_pknorm_i16_f32 v6, v228, v229
	v_cvt_pknorm_i16_f32 v7, v230, v231
	v_pk_mul_f32 v[224:225], v[30:31], v[2:3] op_sel:[0,1] op_sel_hi:[1,1]
	v_pk_mul_f32 v[226:227], v[32:33], v[2:3] op_sel:[0,1] op_sel_hi:[1,1]
	v_cvt_pknorm_i16_f32 v8, v224, v225
	s_waitcnt lgkmcnt(0)
	v_max_f32_e32 v13, v13, v44
	v_cvt_pknorm_i16_f32 v9, v226, v227
	v_rcp_f32_e32 v3, v13
	v_cmp_lt_f32_e32 vcc, 0, v13
	s_mov_b64 s[6:7], 0x3400
	v_lshl_add_u64 v[10:11], v[4:5], 0, s[6:7]
	v_cndmask_b32_e32 v3, 0, v3, vcc
	global_store_dwordx4 v[10:11], v[6:9], off sc0 sc1
	s_nop 1
	v_pk_mul_f32 v[228:229], v[34:35], v[2:3] op_sel:[0,1] op_sel_hi:[1,1]
	v_pk_mul_f32 v[230:231], v[36:37], v[2:3] op_sel:[0,1] op_sel_hi:[1,1]
	v_cvt_pknorm_i16_f32 v6, v228, v229
	v_cvt_pknorm_i16_f32 v7, v230, v231
	v_pk_mul_f32 v[224:225], v[38:39], v[2:3] op_sel:[0,1] op_sel_hi:[1,1]
	v_pk_mul_f32 v[226:227], v[40:41], v[2:3] op_sel:[0,1] op_sel_hi:[1,1]
	v_cvt_pknorm_i16_f32 v8, v224, v225
	s_mov_b64 s[6:7], 0x3600
	v_cvt_pknorm_i16_f32 v9, v226, v227
	v_lshl_add_u64 v[10:11], v[4:5], 0, s[6:7]
	global_store_dwordx4 v[10:11], v[6:9], off sc0 sc1
	s_nop 1
	v_pk_mul_f32 v[6:7], v[12:13], s[4:5] op_sel_hi:[1,0]
	global_store_dwordx2 v0, v[6:7], s[2:3] offset:104
	v_accvgpr_read_b32 v3, a0
	v_accvgpr_read_b32 v6, a16
	v_accvgpr_read_b32 v7, a32
	v_max3_f32 v8, |v3|, |v6|, |v7|
	v_accvgpr_read_b32 v9, a48
	v_accvgpr_read_b32 v14, a64
	v_max3_f32 v8, |v8|, |v9|, |v14|
	v_accvgpr_read_b32 v15, a112
	v_accvgpr_read_b32 v16, a128
	v_max3_f32 v8, |v8|, |v15|, |v16|
	v_accvgpr_read_b32 v10, a80
	v_accvgpr_read_b32 v17, a80
	v_max3_f32 v8, |v8|, |v17|, |v10|
	v_accvgpr_read_b32 v18, a1
	v_accvgpr_read_b32 v19, a17
	v_accvgpr_read_b32 v20, a33
	v_max3_f32 v10, |v18|, |v19|, |v20|
	v_accvgpr_read_b32 v21, a49
	v_accvgpr_read_b32 v22, a65
	v_max3_f32 v10, |v10|, |v21|, |v22|
	v_accvgpr_read_b32 v23, a113
	v_accvgpr_read_b32 v24, a129
	v_max3_f32 v10, |v10|, |v23|, |v24|
	v_accvgpr_read_b32 v11, a81
	v_accvgpr_read_b32 v25, a81
	v_max3_f32 v11, |v10|, |v25|, |v11|
	v_accvgpr_read_b32 v26, a2
	v_accvgpr_read_b32 v27, a18
	v_accvgpr_read_b32 v28, a34
	v_max3_f32 v10, |v26|, |v27|, |v28|
	v_accvgpr_read_b32 v29, a50
	v_accvgpr_read_b32 v30, a66
	v_max3_f32 v10, |v10|, |v29|, |v30|
	v_accvgpr_read_b32 v31, a114
	v_accvgpr_read_b32 v32, a130
	v_max3_f32 v10, |v10|, |v31|, |v32|
	v_accvgpr_read_b32 v12, a82
	v_accvgpr_read_b32 v33, a82
	v_max3_f32 v12, |v10|, |v33|, |v12|
	v_accvgpr_read_b32 v34, a3
	v_accvgpr_read_b32 v35, a19
	v_accvgpr_read_b32 v36, a35
	v_max3_f32 v10, |v34|, |v35|, |v36|
	v_accvgpr_read_b32 v37, a51
	v_accvgpr_read_b32 v38, a67
	v_max3_f32 v10, |v10|, |v37|, |v38|
	v_accvgpr_read_b32 v13, a83
	v_accvgpr_read_b32 v39, a115
	v_accvgpr_read_b32 v40, a131
	v_max3_f32 v10, |v10|, |v39|, |v40|
	v_accvgpr_read_b32 v41, a83
	v_max3_f32 v13, |v10|, |v41|, |v13|
	s_mov_b64 s[6:7], 0x4000
	s_nop 1
	v_max_f32_dpp v8, v8, v8 quad_perm:[1,0,3,2] row_mask:0xf bank_mask:0xf
	v_max_f32_dpp v11, v11, v11 quad_perm:[1,0,3,2] row_mask:0xf bank_mask:0xf
	v_max_f32_dpp v12, v12, v12 quad_perm:[1,0,3,2] row_mask:0xf bank_mask:0xf
	v_max_f32_dpp v13, v13, v13 quad_perm:[1,0,3,2] row_mask:0xf bank_mask:0xf
	v_max_f32_dpp v8, v8, v8 quad_perm:[2,3,0,1] row_mask:0xf bank_mask:0xf
	v_max_f32_dpp v11, v11, v11 quad_perm:[2,3,0,1] row_mask:0xf bank_mask:0xf
	v_max_f32_dpp v12, v12, v12 quad_perm:[2,3,0,1] row_mask:0xf bank_mask:0xf
	v_max_f32_dpp v13, v13, v13 quad_perm:[2,3,0,1] row_mask:0xf bank_mask:0xf
	v_max_f32_dpp v8, v8, v8 row_half_mirror row_mask:0xf bank_mask:0xf
	v_max_f32_dpp v11, v11, v11 row_half_mirror row_mask:0xf bank_mask:0xf
	v_max_f32_dpp v12, v12, v12 row_half_mirror row_mask:0xf bank_mask:0xf
	v_max_f32_dpp v13, v13, v13 row_half_mirror row_mask:0xf bank_mask:0xf
	v_max_f32_dpp v8, v8, v8 row_mirror row_mask:0xf bank_mask:0xf
	v_max_f32_dpp v11, v11, v11 row_mirror row_mask:0xf bank_mask:0xf
	v_max_f32_dpp v12, v12, v12 row_mirror row_mask:0xf bank_mask:0xf
	v_max_f32_dpp v13, v13, v13 row_mirror row_mask:0xf bank_mask:0xf
	s_nop 0
	ds_swizzle_b32 v10, v8 offset:swizzle(SWAP,16)
	s_waitcnt lgkmcnt(0)
	v_max_f32_e32 v10, v8, v10
	ds_swizzle_b32 v42, v11 offset:swizzle(SWAP,16)
	v_rcp_f32_e32 v8, v10
	v_cmp_lt_f32_e32 vcc, 0, v10
	s_waitcnt lgkmcnt(0)
	v_max_f32_e32 v11, v11, v42
	ds_swizzle_b32 v43, v12 offset:swizzle(SWAP,16)
	s_waitcnt lgkmcnt(0)
	v_max_f32_e32 v12, v12, v43
	ds_swizzle_b32 v44, v13 offset:swizzle(SWAP,16)
	v_cndmask_b32_e32 v42, 0, v8, vcc
	v_mul_f32_e32 v3, v42, v3
	v_mul_f32_e32 v6, v42, v6
	v_cvt_pknorm_i16_f32 v6, v3, v6
	v_mul_f32_e32 v3, v42, v7
	v_mul_f32_e32 v7, v42, v9
	v_cvt_pknorm_i16_f32 v7, v3, v7
	v_pk_mul_f32 v[228:229], v[14:15], v[42:43] op_sel_hi:[1,0]
	v_pk_mul_f32 v[230:231], v[16:17], v[42:43] op_sel_hi:[1,0]
	v_cvt_pknorm_i16_f32 v8, v228, v229
	v_cvt_pknorm_i16_f32 v9, v230, v231
	v_rcp_f32_e32 v3, v11
	v_cmp_lt_f32_e32 vcc, 0, v11
	v_lshl_add_u64 v[14:15], v[4:5], 0, s[6:7]
	global_store_dwordx4 v[14:15], v[6:9], off sc0 sc1
	s_nop 1
	s_mov_b64 s[6:7], 0x4200
	v_cndmask_b32_e32 v3, 0, v3, vcc
	v_pk_mul_f32 v[224:225], v[18:19], v[2:3] op_sel:[0,1] op_sel_hi:[1,1]
	v_pk_mul_f32 v[226:227], v[20:21], v[2:3] op_sel:[0,1] op_sel_hi:[1,1]
	v_cvt_pknorm_i16_f32 v6, v224, v225
	v_cvt_pknorm_i16_f32 v7, v226, v227
	v_pk_mul_f32 v[228:229], v[22:23], v[2:3] op_sel:[0,1] op_sel_hi:[1,1]
	v_pk_mul_f32 v[230:231], v[24:25], v[2:3] op_sel:[0,1] op_sel_hi:[1,1]
	v_cvt_pknorm_i16_f32 v8, v228, v229
	v_cvt_pknorm_i16_f32 v9, v230, v231
	v_rcp_f32_e32 v3, v12
	v_cmp_lt_f32_e32 vcc, 0, v12
	v_lshl_add_u64 v[14:15], v[4:5], 0, s[6:7]
	global_store_dwordx4 v[14:15], v[6:9], off sc0 sc1
	s_nop 1
	v_pk_mul_f32 v[6:7], v[10:11], s[4:5] op_sel_hi:[1,0]
	v_cndmask_b32_e32 v3, 0, v3, vcc
	global_store_dwordx2 v0, v[6:7], s[2:3] offset:128
	v_pk_mul_f32 v[224:225], v[26:27], v[2:3] op_sel:[0,1] op_sel_hi:[1,1]
	v_pk_mul_f32 v[226:227], v[28:29], v[2:3] op_sel:[0,1] op_sel_hi:[1,1]
	v_cvt_pknorm_i16_f32 v6, v224, v225
	v_cvt_pknorm_i16_f32 v7, v226, v227
	v_pk_mul_f32 v[228:229], v[30:31], v[2:3] op_sel:[0,1] op_sel_hi:[1,1]
	v_pk_mul_f32 v[230:231], v[32:33], v[2:3] op_sel:[0,1] op_sel_hi:[1,1]
	v_cvt_pknorm_i16_f32 v8, v228, v229
	s_waitcnt lgkmcnt(0)
	v_max_f32_e32 v13, v13, v44
	v_cvt_pknorm_i16_f32 v9, v230, v231
	v_rcp_f32_e32 v3, v13
	v_cmp_lt_f32_e32 vcc, 0, v13
	s_mov_b64 s[6:7], 0x4400
	v_lshl_add_u64 v[10:11], v[4:5], 0, s[6:7]
	v_cndmask_b32_e32 v3, 0, v3, vcc
	global_store_dwordx4 v[10:11], v[6:9], off sc0 sc1
	s_nop 1
	v_pk_mul_f32 v[224:225], v[34:35], v[2:3] op_sel:[0,1] op_sel_hi:[1,1]
	v_pk_mul_f32 v[226:227], v[36:37], v[2:3] op_sel:[0,1] op_sel_hi:[1,1]
	v_cvt_pknorm_i16_f32 v6, v224, v225
	v_cvt_pknorm_i16_f32 v7, v226, v227
	v_pk_mul_f32 v[228:229], v[38:39], v[2:3] op_sel:[0,1] op_sel_hi:[1,1]
	v_pk_mul_f32 v[230:231], v[40:41], v[2:3] op_sel:[0,1] op_sel_hi:[1,1]
	v_cvt_pknorm_i16_f32 v8, v228, v229
	s_mov_b64 s[6:7], 0x4600
	v_cvt_pknorm_i16_f32 v9, v230, v231
	v_lshl_add_u64 v[10:11], v[4:5], 0, s[6:7]
	global_store_dwordx4 v[10:11], v[6:9], off sc0 sc1
	s_nop 1
	v_pk_mul_f32 v[6:7], v[12:13], s[4:5] op_sel_hi:[1,0]
	global_store_dwordx2 v0, v[6:7], s[2:3] offset:136
	v_accvgpr_read_b32 v3, a4
	v_accvgpr_read_b32 v6, a20
	v_accvgpr_read_b32 v7, a36
	v_max3_f32 v8, |v3|, |v6|, |v7|
	v_accvgpr_read_b32 v9, a52
	v_accvgpr_read_b32 v14, a68
	v_max3_f32 v8, |v8|, |v9|, |v14|
	v_accvgpr_read_b32 v15, a116
	v_accvgpr_read_b32 v16, a132
	v_max3_f32 v8, |v8|, |v15|, |v16|
	v_accvgpr_read_b32 v10, a84
	v_accvgpr_read_b32 v17, a84
	v_max3_f32 v8, |v8|, |v17|, |v10|
	v_accvgpr_read_b32 v18, a5
	v_accvgpr_read_b32 v19, a21
	v_accvgpr_read_b32 v20, a37
	v_max3_f32 v10, |v18|, |v19|, |v20|
	v_accvgpr_read_b32 v21, a53
	v_accvgpr_read_b32 v22, a69
	v_max3_f32 v10, |v10|, |v21|, |v22|
	v_accvgpr_read_b32 v23, a117
	v_accvgpr_read_b32 v24, a133
	v_max3_f32 v10, |v10|, |v23|, |v24|
	v_accvgpr_read_b32 v11, a85
	v_accvgpr_read_b32 v25, a85
	v_max3_f32 v11, |v10|, |v25|, |v11|
	v_accvgpr_read_b32 v26, a6
	v_accvgpr_read_b32 v27, a22
	v_accvgpr_read_b32 v28, a38
	v_max3_f32 v10, |v26|, |v27|, |v28|
	v_accvgpr_read_b32 v29, a54
	v_accvgpr_read_b32 v30, a70
	v_max3_f32 v10, |v10|, |v29|, |v30|
	v_accvgpr_read_b32 v31, a118
	v_accvgpr_read_b32 v32, a134
	v_max3_f32 v10, |v10|, |v31|, |v32|
	v_accvgpr_read_b32 v12, a86
	v_accvgpr_read_b32 v33, a86
	v_max3_f32 v12, |v10|, |v33|, |v12|
	v_accvgpr_read_b32 v34, a7
	v_accvgpr_read_b32 v35, a23
	v_accvgpr_read_b32 v36, a39
	v_max3_f32 v10, |v34|, |v35|, |v36|
	v_accvgpr_read_b32 v37, a55
	v_accvgpr_read_b32 v38, a71
	v_max3_f32 v10, |v10|, |v37|, |v38|
	v_accvgpr_read_b32 v13, a87
	v_accvgpr_read_b32 v39, a119
	v_accvgpr_read_b32 v40, a135
	v_max3_f32 v10, |v10|, |v39|, |v40|
	v_accvgpr_read_b32 v41, a87
	v_max3_f32 v13, |v10|, |v41|, |v13|
	s_mov_b64 s[6:7], 0x5000
	s_nop 1
	v_max_f32_dpp v8, v8, v8 quad_perm:[1,0,3,2] row_mask:0xf bank_mask:0xf
	v_max_f32_dpp v11, v11, v11 quad_perm:[1,0,3,2] row_mask:0xf bank_mask:0xf
	v_max_f32_dpp v12, v12, v12 quad_perm:[1,0,3,2] row_mask:0xf bank_mask:0xf
	v_max_f32_dpp v13, v13, v13 quad_perm:[1,0,3,2] row_mask:0xf bank_mask:0xf
	v_max_f32_dpp v8, v8, v8 quad_perm:[2,3,0,1] row_mask:0xf bank_mask:0xf
	v_max_f32_dpp v11, v11, v11 quad_perm:[2,3,0,1] row_mask:0xf bank_mask:0xf
	v_max_f32_dpp v12, v12, v12 quad_perm:[2,3,0,1] row_mask:0xf bank_mask:0xf
	v_max_f32_dpp v13, v13, v13 quad_perm:[2,3,0,1] row_mask:0xf bank_mask:0xf
	v_max_f32_dpp v8, v8, v8 row_half_mirror row_mask:0xf bank_mask:0xf
	v_max_f32_dpp v11, v11, v11 row_half_mirror row_mask:0xf bank_mask:0xf
	v_max_f32_dpp v12, v12, v12 row_half_mirror row_mask:0xf bank_mask:0xf
	v_max_f32_dpp v13, v13, v13 row_half_mirror row_mask:0xf bank_mask:0xf
	v_max_f32_dpp v8, v8, v8 row_mirror row_mask:0xf bank_mask:0xf
	v_max_f32_dpp v11, v11, v11 row_mirror row_mask:0xf bank_mask:0xf
	v_max_f32_dpp v12, v12, v12 row_mirror row_mask:0xf bank_mask:0xf
	v_max_f32_dpp v13, v13, v13 row_mirror row_mask:0xf bank_mask:0xf
	s_nop 0
	ds_swizzle_b32 v10, v8 offset:swizzle(SWAP,16)
	s_waitcnt lgkmcnt(0)
	v_max_f32_e32 v10, v8, v10
	ds_swizzle_b32 v42, v11 offset:swizzle(SWAP,16)
	v_rcp_f32_e32 v8, v10
	v_cmp_lt_f32_e32 vcc, 0, v10
	s_waitcnt lgkmcnt(0)
	v_max_f32_e32 v11, v11, v42
	ds_swizzle_b32 v43, v12 offset:swizzle(SWAP,16)
	s_waitcnt lgkmcnt(0)
	v_max_f32_e32 v12, v12, v43
	ds_swizzle_b32 v44, v13 offset:swizzle(SWAP,16)
	v_cndmask_b32_e32 v42, 0, v8, vcc
	v_mul_f32_e32 v3, v42, v3
	v_mul_f32_e32 v6, v42, v6
	v_cvt_pknorm_i16_f32 v6, v3, v6
	v_mul_f32_e32 v3, v42, v7
	v_mul_f32_e32 v7, v42, v9
	v_cvt_pknorm_i16_f32 v7, v3, v7
	v_pk_mul_f32 v[224:225], v[14:15], v[42:43] op_sel_hi:[1,0]
	v_pk_mul_f32 v[226:227], v[16:17], v[42:43] op_sel_hi:[1,0]
	v_cvt_pknorm_i16_f32 v8, v224, v225
	v_cvt_pknorm_i16_f32 v9, v226, v227
	v_rcp_f32_e32 v3, v11
	v_cmp_lt_f32_e32 vcc, 0, v11
	v_lshl_add_u64 v[14:15], v[4:5], 0, s[6:7]
	global_store_dwordx4 v[14:15], v[6:9], off sc0 sc1
	s_nop 1
	s_mov_b64 s[6:7], 0x5200
	v_cndmask_b32_e32 v3, 0, v3, vcc
	v_pk_mul_f32 v[228:229], v[18:19], v[2:3] op_sel:[0,1] op_sel_hi:[1,1]
	v_pk_mul_f32 v[230:231], v[20:21], v[2:3] op_sel:[0,1] op_sel_hi:[1,1]
	v_cvt_pknorm_i16_f32 v6, v228, v229
	v_cvt_pknorm_i16_f32 v7, v230, v231
	v_pk_mul_f32 v[224:225], v[22:23], v[2:3] op_sel:[0,1] op_sel_hi:[1,1]
	v_pk_mul_f32 v[226:227], v[24:25], v[2:3] op_sel:[0,1] op_sel_hi:[1,1]
	v_cvt_pknorm_i16_f32 v8, v224, v225
	v_cvt_pknorm_i16_f32 v9, v226, v227
	v_rcp_f32_e32 v3, v12
	v_cmp_lt_f32_e32 vcc, 0, v12
	v_lshl_add_u64 v[14:15], v[4:5], 0, s[6:7]
	global_store_dwordx4 v[14:15], v[6:9], off sc0 sc1
	s_nop 1
	v_pk_mul_f32 v[6:7], v[10:11], s[4:5] op_sel_hi:[1,0]
	v_cndmask_b32_e32 v3, 0, v3, vcc
	global_store_dwordx2 v0, v[6:7], s[2:3] offset:160
	v_pk_mul_f32 v[228:229], v[26:27], v[2:3] op_sel:[0,1] op_sel_hi:[1,1]
	v_pk_mul_f32 v[230:231], v[28:29], v[2:3] op_sel:[0,1] op_sel_hi:[1,1]
	v_cvt_pknorm_i16_f32 v6, v228, v229
	v_cvt_pknorm_i16_f32 v7, v230, v231
	v_pk_mul_f32 v[224:225], v[30:31], v[2:3] op_sel:[0,1] op_sel_hi:[1,1]
	v_pk_mul_f32 v[226:227], v[32:33], v[2:3] op_sel:[0,1] op_sel_hi:[1,1]
	v_cvt_pknorm_i16_f32 v8, v224, v225
	s_waitcnt lgkmcnt(0)
	v_max_f32_e32 v13, v13, v44
	v_cvt_pknorm_i16_f32 v9, v226, v227
	v_rcp_f32_e32 v3, v13
	v_cmp_lt_f32_e32 vcc, 0, v13
	s_mov_b64 s[6:7], 0x5400
	v_lshl_add_u64 v[10:11], v[4:5], 0, s[6:7]
	v_cndmask_b32_e32 v3, 0, v3, vcc
	global_store_dwordx4 v[10:11], v[6:9], off sc0 sc1
	s_nop 1
	v_pk_mul_f32 v[228:229], v[34:35], v[2:3] op_sel:[0,1] op_sel_hi:[1,1]
	v_pk_mul_f32 v[230:231], v[36:37], v[2:3] op_sel:[0,1] op_sel_hi:[1,1]
	v_cvt_pknorm_i16_f32 v6, v228, v229
	v_cvt_pknorm_i16_f32 v7, v230, v231
	v_pk_mul_f32 v[224:225], v[38:39], v[2:3] op_sel:[0,1] op_sel_hi:[1,1]
	v_pk_mul_f32 v[226:227], v[40:41], v[2:3] op_sel:[0,1] op_sel_hi:[1,1]
	v_cvt_pknorm_i16_f32 v8, v224, v225
	s_mov_b64 s[6:7], 0x5600
	v_cvt_pknorm_i16_f32 v9, v226, v227
	v_lshl_add_u64 v[10:11], v[4:5], 0, s[6:7]
	global_store_dwordx4 v[10:11], v[6:9], off sc0 sc1
	s_nop 1
	v_pk_mul_f32 v[6:7], v[12:13], s[4:5] op_sel_hi:[1,0]
	global_store_dwordx2 v0, v[6:7], s[2:3] offset:168
	v_accvgpr_read_b32 v3, a8
	v_accvgpr_read_b32 v6, a24
	v_accvgpr_read_b32 v7, a40
	v_max3_f32 v8, |v3|, |v6|, |v7|
	v_accvgpr_read_b32 v9, a56
	v_accvgpr_read_b32 v14, a72
	v_max3_f32 v8, |v8|, |v9|, |v14|
	v_accvgpr_read_b32 v15, a120
	v_accvgpr_read_b32 v16, a136
	v_max3_f32 v8, |v8|, |v15|, |v16|
	v_accvgpr_read_b32 v10, a88
	v_accvgpr_read_b32 v17, a88
	v_max3_f32 v8, |v8|, |v17|, |v10|
	v_accvgpr_read_b32 v18, a9
	v_accvgpr_read_b32 v19, a25
	v_accvgpr_read_b32 v20, a41
	v_max3_f32 v10, |v18|, |v19|, |v20|
	v_accvgpr_read_b32 v21, a57
	v_accvgpr_read_b32 v22, a73
	v_max3_f32 v10, |v10|, |v21|, |v22|
	v_accvgpr_read_b32 v23, a121
	v_accvgpr_read_b32 v24, a137
	v_max3_f32 v10, |v10|, |v23|, |v24|
	v_accvgpr_read_b32 v11, a89
	v_accvgpr_read_b32 v25, a89
	v_max3_f32 v11, |v10|, |v25|, |v11|
	v_accvgpr_read_b32 v26, a10
	v_accvgpr_read_b32 v27, a26
	v_accvgpr_read_b32 v28, a42
	v_max3_f32 v10, |v26|, |v27|, |v28|
	v_accvgpr_read_b32 v29, a58
	v_accvgpr_read_b32 v30, a74
	v_max3_f32 v10, |v10|, |v29|, |v30|
	v_accvgpr_read_b32 v31, a122
	v_accvgpr_read_b32 v32, a138
	v_max3_f32 v10, |v10|, |v31|, |v32|
	v_accvgpr_read_b32 v12, a90
	v_accvgpr_read_b32 v33, a90
	v_max3_f32 v12, |v10|, |v33|, |v12|
	v_accvgpr_read_b32 v34, a11
	v_accvgpr_read_b32 v35, a27
	v_accvgpr_read_b32 v36, a43
	v_max3_f32 v10, |v34|, |v35|, |v36|
	v_accvgpr_read_b32 v37, a59
	v_accvgpr_read_b32 v38, a75
	v_max3_f32 v10, |v10|, |v37|, |v38|
	v_accvgpr_read_b32 v13, a91
	v_accvgpr_read_b32 v39, a123
	v_accvgpr_read_b32 v40, a139
	v_max3_f32 v10, |v10|, |v39|, |v40|
	v_accvgpr_read_b32 v41, a91
	v_max3_f32 v13, |v10|, |v41|, |v13|
	s_mov_b64 s[6:7], 0x6000
	s_nop 1
	v_max_f32_dpp v8, v8, v8 quad_perm:[1,0,3,2] row_mask:0xf bank_mask:0xf
	v_max_f32_dpp v11, v11, v11 quad_perm:[1,0,3,2] row_mask:0xf bank_mask:0xf
	v_max_f32_dpp v12, v12, v12 quad_perm:[1,0,3,2] row_mask:0xf bank_mask:0xf
	v_max_f32_dpp v13, v13, v13 quad_perm:[1,0,3,2] row_mask:0xf bank_mask:0xf
	v_max_f32_dpp v8, v8, v8 quad_perm:[2,3,0,1] row_mask:0xf bank_mask:0xf
	v_max_f32_dpp v11, v11, v11 quad_perm:[2,3,0,1] row_mask:0xf bank_mask:0xf
	v_max_f32_dpp v12, v12, v12 quad_perm:[2,3,0,1] row_mask:0xf bank_mask:0xf
	v_max_f32_dpp v13, v13, v13 quad_perm:[2,3,0,1] row_mask:0xf bank_mask:0xf
	v_max_f32_dpp v8, v8, v8 row_half_mirror row_mask:0xf bank_mask:0xf
	v_max_f32_dpp v11, v11, v11 row_half_mirror row_mask:0xf bank_mask:0xf
	v_max_f32_dpp v12, v12, v12 row_half_mirror row_mask:0xf bank_mask:0xf
	v_max_f32_dpp v13, v13, v13 row_half_mirror row_mask:0xf bank_mask:0xf
	v_max_f32_dpp v8, v8, v8 row_mirror row_mask:0xf bank_mask:0xf
	v_max_f32_dpp v11, v11, v11 row_mirror row_mask:0xf bank_mask:0xf
	v_max_f32_dpp v12, v12, v12 row_mirror row_mask:0xf bank_mask:0xf
	v_max_f32_dpp v13, v13, v13 row_mirror row_mask:0xf bank_mask:0xf
	s_nop 0
	ds_swizzle_b32 v10, v8 offset:swizzle(SWAP,16)
	s_waitcnt lgkmcnt(0)
	v_max_f32_e32 v10, v8, v10
	ds_swizzle_b32 v42, v11 offset:swizzle(SWAP,16)
	v_rcp_f32_e32 v8, v10
	v_cmp_lt_f32_e32 vcc, 0, v10
	s_waitcnt lgkmcnt(0)
	v_max_f32_e32 v11, v11, v42
	ds_swizzle_b32 v43, v12 offset:swizzle(SWAP,16)
	s_waitcnt lgkmcnt(0)
	v_max_f32_e32 v12, v12, v43
	ds_swizzle_b32 v44, v13 offset:swizzle(SWAP,16)
	v_cndmask_b32_e32 v42, 0, v8, vcc
	v_mul_f32_e32 v3, v42, v3
	v_mul_f32_e32 v6, v42, v6
	v_cvt_pknorm_i16_f32 v6, v3, v6
	v_mul_f32_e32 v3, v42, v7
	v_mul_f32_e32 v7, v42, v9
	v_cvt_pknorm_i16_f32 v7, v3, v7
	v_pk_mul_f32 v[228:229], v[14:15], v[42:43] op_sel_hi:[1,0]
	v_pk_mul_f32 v[230:231], v[16:17], v[42:43] op_sel_hi:[1,0]
	v_cvt_pknorm_i16_f32 v8, v228, v229
	v_cvt_pknorm_i16_f32 v9, v230, v231
	v_rcp_f32_e32 v3, v11
	v_cmp_lt_f32_e32 vcc, 0, v11
	v_lshl_add_u64 v[14:15], v[4:5], 0, s[6:7]
	global_store_dwordx4 v[14:15], v[6:9], off sc0 sc1
	s_nop 1
	s_mov_b64 s[6:7], 0x6200
	v_cndmask_b32_e32 v3, 0, v3, vcc
	v_pk_mul_f32 v[224:225], v[18:19], v[2:3] op_sel:[0,1] op_sel_hi:[1,1]
	v_pk_mul_f32 v[226:227], v[20:21], v[2:3] op_sel:[0,1] op_sel_hi:[1,1]
	v_cvt_pknorm_i16_f32 v6, v224, v225
	v_cvt_pknorm_i16_f32 v7, v226, v227
	v_pk_mul_f32 v[228:229], v[22:23], v[2:3] op_sel:[0,1] op_sel_hi:[1,1]
	v_pk_mul_f32 v[230:231], v[24:25], v[2:3] op_sel:[0,1] op_sel_hi:[1,1]
	v_cvt_pknorm_i16_f32 v8, v228, v229
	v_cvt_pknorm_i16_f32 v9, v230, v231
	v_rcp_f32_e32 v3, v12
	v_cmp_lt_f32_e32 vcc, 0, v12
	v_lshl_add_u64 v[14:15], v[4:5], 0, s[6:7]
	global_store_dwordx4 v[14:15], v[6:9], off sc0 sc1
	s_nop 1
	v_pk_mul_f32 v[6:7], v[10:11], s[4:5] op_sel_hi:[1,0]
	v_cndmask_b32_e32 v3, 0, v3, vcc
	global_store_dwordx2 v0, v[6:7], s[2:3] offset:192
	v_pk_mul_f32 v[224:225], v[26:27], v[2:3] op_sel:[0,1] op_sel_hi:[1,1]
	v_pk_mul_f32 v[226:227], v[28:29], v[2:3] op_sel:[0,1] op_sel_hi:[1,1]
	v_cvt_pknorm_i16_f32 v6, v224, v225
	v_cvt_pknorm_i16_f32 v7, v226, v227
	v_pk_mul_f32 v[228:229], v[30:31], v[2:3] op_sel:[0,1] op_sel_hi:[1,1]
	v_pk_mul_f32 v[230:231], v[32:33], v[2:3] op_sel:[0,1] op_sel_hi:[1,1]
	v_cvt_pknorm_i16_f32 v8, v228, v229
	s_waitcnt lgkmcnt(0)
	v_max_f32_e32 v13, v13, v44
	v_cvt_pknorm_i16_f32 v9, v230, v231
	v_rcp_f32_e32 v3, v13
	v_cmp_lt_f32_e32 vcc, 0, v13
	s_mov_b64 s[6:7], 0x6400
	v_lshl_add_u64 v[10:11], v[4:5], 0, s[6:7]
	v_cndmask_b32_e32 v3, 0, v3, vcc
	global_store_dwordx4 v[10:11], v[6:9], off sc0 sc1
	s_nop 1
	v_pk_mul_f32 v[224:225], v[34:35], v[2:3] op_sel:[0,1] op_sel_hi:[1,1]
	v_pk_mul_f32 v[226:227], v[36:37], v[2:3] op_sel:[0,1] op_sel_hi:[1,1]
	v_cvt_pknorm_i16_f32 v6, v224, v225
	v_cvt_pknorm_i16_f32 v7, v226, v227
	v_pk_mul_f32 v[228:229], v[38:39], v[2:3] op_sel:[0,1] op_sel_hi:[1,1]
	v_pk_mul_f32 v[230:231], v[40:41], v[2:3] op_sel:[0,1] op_sel_hi:[1,1]
	v_cvt_pknorm_i16_f32 v8, v228, v229
	s_mov_b64 s[6:7], 0x6600
	v_cvt_pknorm_i16_f32 v9, v230, v231
	v_lshl_add_u64 v[10:11], v[4:5], 0, s[6:7]
	global_store_dwordx4 v[10:11], v[6:9], off sc0 sc1
	s_nop 1
	v_pk_mul_f32 v[6:7], v[12:13], s[4:5] op_sel_hi:[1,0]
	global_store_dwordx2 v0, v[6:7], s[2:3] offset:200
	v_accvgpr_read_b32 v3, a12
	v_accvgpr_read_b32 v6, a28
	v_accvgpr_read_b32 v7, a44
	v_max3_f32 v8, |v3|, |v6|, |v7|
	v_accvgpr_read_b32 v9, a60
	v_accvgpr_read_b32 v14, a76
	v_max3_f32 v8, |v8|, |v9|, |v14|
	v_accvgpr_read_b32 v15, a124
	v_accvgpr_read_b32 v16, a140
	v_max3_f32 v8, |v8|, |v15|, |v16|
	v_accvgpr_read_b32 v10, a92
	v_accvgpr_read_b32 v17, a92
	v_max3_f32 v8, |v8|, |v17|, |v10|
	v_accvgpr_read_b32 v18, a13
	v_accvgpr_read_b32 v19, a29
	v_accvgpr_read_b32 v20, a45
	v_max3_f32 v10, |v18|, |v19|, |v20|
	v_accvgpr_read_b32 v21, a61
	v_accvgpr_read_b32 v22, a77
	v_max3_f32 v10, |v10|, |v21|, |v22|
	v_accvgpr_read_b32 v23, a125
	v_accvgpr_read_b32 v24, a141
	v_max3_f32 v10, |v10|, |v23|, |v24|
	v_accvgpr_read_b32 v11, a93
	v_accvgpr_read_b32 v25, a93
	v_max3_f32 v11, |v10|, |v25|, |v11|
	v_accvgpr_read_b32 v26, a14
	v_accvgpr_read_b32 v27, a30
	v_accvgpr_read_b32 v28, a46
	v_max3_f32 v10, |v26|, |v27|, |v28|
	v_accvgpr_read_b32 v29, a62
	v_accvgpr_read_b32 v30, a78
	v_max3_f32 v10, |v10|, |v29|, |v30|
	v_accvgpr_read_b32 v31, a126
	v_accvgpr_read_b32 v32, a142
	v_max3_f32 v10, |v10|, |v31|, |v32|
	v_accvgpr_read_b32 v12, a94
	v_accvgpr_read_b32 v33, a94
	v_max3_f32 v12, |v10|, |v33|, |v12|
	v_accvgpr_read_b32 v34, a15
	v_accvgpr_read_b32 v35, a31
	v_accvgpr_read_b32 v36, a47
	v_max3_f32 v10, |v34|, |v35|, |v36|
	v_accvgpr_read_b32 v37, a63
	v_accvgpr_read_b32 v38, a79
	v_max3_f32 v10, |v10|, |v37|, |v38|
	v_accvgpr_read_b32 v13, a95
	v_accvgpr_read_b32 v39, a127
	v_accvgpr_read_b32 v40, a143
	v_max3_f32 v10, |v10|, |v39|, |v40|
	v_accvgpr_read_b32 v41, a95
	v_max3_f32 v13, |v10|, |v41|, |v13|
	s_mov_b64 s[6:7], 0x7000
	s_nop 1
	v_max_f32_dpp v8, v8, v8 quad_perm:[1,0,3,2] row_mask:0xf bank_mask:0xf
	v_max_f32_dpp v11, v11, v11 quad_perm:[1,0,3,2] row_mask:0xf bank_mask:0xf
	v_max_f32_dpp v12, v12, v12 quad_perm:[1,0,3,2] row_mask:0xf bank_mask:0xf
	v_max_f32_dpp v13, v13, v13 quad_perm:[1,0,3,2] row_mask:0xf bank_mask:0xf
	v_max_f32_dpp v8, v8, v8 quad_perm:[2,3,0,1] row_mask:0xf bank_mask:0xf
	v_max_f32_dpp v11, v11, v11 quad_perm:[2,3,0,1] row_mask:0xf bank_mask:0xf
	v_max_f32_dpp v12, v12, v12 quad_perm:[2,3,0,1] row_mask:0xf bank_mask:0xf
	v_max_f32_dpp v13, v13, v13 quad_perm:[2,3,0,1] row_mask:0xf bank_mask:0xf
	v_max_f32_dpp v8, v8, v8 row_half_mirror row_mask:0xf bank_mask:0xf
	v_max_f32_dpp v11, v11, v11 row_half_mirror row_mask:0xf bank_mask:0xf
	v_max_f32_dpp v12, v12, v12 row_half_mirror row_mask:0xf bank_mask:0xf
	v_max_f32_dpp v13, v13, v13 row_half_mirror row_mask:0xf bank_mask:0xf
	v_max_f32_dpp v8, v8, v8 row_mirror row_mask:0xf bank_mask:0xf
	v_max_f32_dpp v11, v11, v11 row_mirror row_mask:0xf bank_mask:0xf
	v_max_f32_dpp v12, v12, v12 row_mirror row_mask:0xf bank_mask:0xf
	v_max_f32_dpp v13, v13, v13 row_mirror row_mask:0xf bank_mask:0xf
	s_nop 0
	ds_swizzle_b32 v10, v8 offset:swizzle(SWAP,16)
	s_waitcnt lgkmcnt(0)
	v_max_f32_e32 v10, v8, v10
	ds_swizzle_b32 v42, v11 offset:swizzle(SWAP,16)
	v_rcp_f32_e32 v8, v10
	v_cmp_lt_f32_e32 vcc, 0, v10
	s_waitcnt lgkmcnt(0)
	v_max_f32_e32 v11, v11, v42
	ds_swizzle_b32 v43, v12 offset:swizzle(SWAP,16)
	s_waitcnt lgkmcnt(0)
	v_max_f32_e32 v12, v12, v43
	ds_swizzle_b32 v44, v13 offset:swizzle(SWAP,16)
	v_cndmask_b32_e32 v42, 0, v8, vcc
	v_mul_f32_e32 v3, v42, v3
	v_mul_f32_e32 v6, v42, v6
	v_cvt_pknorm_i16_f32 v6, v3, v6
	v_mul_f32_e32 v3, v42, v7
	v_mul_f32_e32 v7, v42, v9
	v_cvt_pknorm_i16_f32 v7, v3, v7
	v_pk_mul_f32 v[224:225], v[14:15], v[42:43] op_sel_hi:[1,0]
	v_pk_mul_f32 v[226:227], v[16:17], v[42:43] op_sel_hi:[1,0]
	v_cvt_pknorm_i16_f32 v8, v224, v225
	v_cvt_pknorm_i16_f32 v9, v226, v227
	v_rcp_f32_e32 v3, v11
	v_cmp_lt_f32_e32 vcc, 0, v11
	v_lshl_add_u64 v[14:15], v[4:5], 0, s[6:7]
	global_store_dwordx4 v[14:15], v[6:9], off sc0 sc1
	s_nop 1
	s_mov_b64 s[6:7], 0x7200
	v_cndmask_b32_e32 v3, 0, v3, vcc
	v_pk_mul_f32 v[228:229], v[18:19], v[2:3] op_sel:[0,1] op_sel_hi:[1,1]
	v_pk_mul_f32 v[230:231], v[20:21], v[2:3] op_sel:[0,1] op_sel_hi:[1,1]
	v_cvt_pknorm_i16_f32 v6, v228, v229
	v_cvt_pknorm_i16_f32 v7, v230, v231
	v_pk_mul_f32 v[224:225], v[22:23], v[2:3] op_sel:[0,1] op_sel_hi:[1,1]
	v_pk_mul_f32 v[226:227], v[24:25], v[2:3] op_sel:[0,1] op_sel_hi:[1,1]
	v_cvt_pknorm_i16_f32 v8, v224, v225
	v_cvt_pknorm_i16_f32 v9, v226, v227
	v_rcp_f32_e32 v3, v12
	v_cmp_lt_f32_e32 vcc, 0, v12
	v_lshl_add_u64 v[14:15], v[4:5], 0, s[6:7]
	global_store_dwordx4 v[14:15], v[6:9], off sc0 sc1
	s_nop 1
	v_pk_mul_f32 v[6:7], v[10:11], s[4:5] op_sel_hi:[1,0]
	v_cndmask_b32_e32 v3, 0, v3, vcc
	global_store_dwordx2 v0, v[6:7], s[2:3] offset:224
	v_pk_mul_f32 v[228:229], v[26:27], v[2:3] op_sel:[0,1] op_sel_hi:[1,1]
	v_pk_mul_f32 v[230:231], v[28:29], v[2:3] op_sel:[0,1] op_sel_hi:[1,1]
	v_cvt_pknorm_i16_f32 v6, v228, v229
	v_cvt_pknorm_i16_f32 v7, v230, v231
	v_pk_mul_f32 v[224:225], v[30:31], v[2:3] op_sel:[0,1] op_sel_hi:[1,1]
	v_pk_mul_f32 v[226:227], v[32:33], v[2:3] op_sel:[0,1] op_sel_hi:[1,1]
	v_cvt_pknorm_i16_f32 v8, v224, v225
	s_waitcnt lgkmcnt(0)
	v_max_f32_e32 v13, v13, v44
	v_cvt_pknorm_i16_f32 v9, v226, v227
	v_rcp_f32_e32 v3, v13
	v_cmp_lt_f32_e32 vcc, 0, v13
	s_mov_b64 s[6:7], 0x7400
	v_lshl_add_u64 v[10:11], v[4:5], 0, s[6:7]
	v_cndmask_b32_e32 v3, 0, v3, vcc
	global_store_dwordx4 v[10:11], v[6:9], off sc0 sc1
	s_nop 1
	v_pk_mul_f32 v[228:229], v[34:35], v[2:3] op_sel:[0,1] op_sel_hi:[1,1]
	v_pk_mul_f32 v[230:231], v[36:37], v[2:3] op_sel:[0,1] op_sel_hi:[1,1]
	v_cvt_pknorm_i16_f32 v6, v228, v229
	v_cvt_pknorm_i16_f32 v7, v230, v231
	v_pk_mul_f32 v[224:225], v[38:39], v[2:3] op_sel:[0,1] op_sel_hi:[1,1]
	v_pk_mul_f32 v[226:227], v[40:41], v[2:3] op_sel:[0,1] op_sel_hi:[1,1]
	v_cvt_pknorm_i16_f32 v8, v224, v225
	s_mov_b64 s[6:7], 0x7600
	v_cvt_pknorm_i16_f32 v9, v226, v227
	v_lshl_add_u64 v[4:5], v[4:5], 0, s[6:7]
	global_store_dwordx4 v[4:5], v[6:9], off sc0 sc1
	s_nop 1
	v_pk_mul_f32 v[4:5], v[12:13], s[4:5] op_sel_hi:[1,0]
	global_store_dwordx2 v0, v[4:5], s[2:3] offset:232
	ds_bpermute_b32 v4, v133, v134
	s_lshl_b64 s[0:1], s[0:1], 2
	s_add_u32 s0, s26, s0
	s_addc_u32 s1, s27, s1
	v_mov_b32_e32 v3, v1
	v_cmp_gt_i32_e32 vcc, 32, v132
	v_lshl_add_u64 v[0:1], s[0:1], 0, v[2:3]
	s_and_saveexec_b64 s[0:1], vcc
	s_cbranch_execz .LBB1_6
	s_waitcnt lgkmcnt(0)
	v_add_f32_e32 v2, v134, v4
	global_store_dword v[0:1], v2, off

	.amdhsa_kernel _Z6k_mainPKDF16_PKfS2_S2_PKmPjPfS6_
		.amdhsa_group_segment_fixed_size 114688
		.amdhsa_private_segment_fixed_size 0
		.amdhsa_kernarg_size 64
		.amdhsa_user_sgpr_count 2
		.amdhsa_user_sgpr_dispatch_ptr 0
		.amdhsa_user_sgpr_queue_ptr 0
		.amdhsa_user_sgpr_kernarg_segment_ptr 1
		.amdhsa_user_sgpr_dispatch_id 0
		.amdhsa_user_sgpr_kernarg_preload_length 0
		.amdhsa_user_sgpr_kernarg_preload_offset 0
		.amdhsa_user_sgpr_private_segment_size 0
		.amdhsa_uses_dynamic_stack 0
		.amdhsa_enable_private_segment 0
		.amdhsa_system_sgpr_workgroup_id_x 1
		.amdhsa_system_sgpr_workgroup_id_y 0
		.amdhsa_system_sgpr_workgroup_id_z 0
		.amdhsa_system_sgpr_workgroup_info 0
		.amdhsa_system_vgpr_workitem_id 0
		.amdhsa_next_free_vgpr 488
		.amdhsa_next_free_sgpr 96
		.amdhsa_accum_offset 232
		.amdhsa_reserve_vcc 1
		.amdhsa_float_round_mode_32 0
		.amdhsa_float_round_mode_16_64 0
		.amdhsa_float_denorm_mode_32 3
		.amdhsa_float_denorm_mode_16_64 3
		.amdhsa_dx10_clamp 1
		.amdhsa_ieee_mode 1
		.amdhsa_fp16_overflow 0
		.amdhsa_tg_split 0
		.amdhsa_exception_fp_ieee_invalid_op 0
		.amdhsa_exception_fp_denorm_src 0
		.amdhsa_exception_fp_ieee_div_zero 0
		.amdhsa_exception_fp_ieee_overflow 0
		.amdhsa_exception_fp_ieee_underflow 0
		.amdhsa_exception_fp_ieee_inexact 0
		.amdhsa_exception_int_div_zero 0
	.end_amdhsa_kernel

amdhsa.kernels:
  - .agpr_count:     0
    .args:
      - .actual_access:  read_only
        .address_space:  global
        .offset:         0
        .size:           8
        .value_kind:     global_buffer
      - .address_space:  global
        .offset:         8
        .size:           8
        .value_kind:     global_buffer
      - .actual_access:  read_only
        .address_space:  global
        .offset:         16
        .size:           8
        .value_kind:     global_buffer
      - .actual_access:  read_only
        .address_space:  global
        .offset:         24
        .size:           8
        .value_kind:     global_buffer
      - .actual_access:  read_only
        .address_space:  global
        .offset:         32
        .size:           8
        .value_kind:     global_buffer
      - .actual_access:  read_only
        .address_space:  global
        .offset:         40
        .size:           8
        .value_kind:     global_buffer
      - .actual_access:  read_only
        .address_space:  global
        .offset:         48
        .size:           8
        .value_kind:     global_buffer
      - .actual_access:  read_only
        .address_space:  global
        .offset:         56
        .size:           8
        .value_kind:     global_buffer
      - .actual_access:  write_only
        .address_space:  global
        .offset:         64
        .size:           8
        .value_kind:     global_buffer
      - .actual_access:  write_only
        .address_space:  global
        .offset:         72
        .size:           8
        .value_kind:     global_buffer
      - .actual_access:  write_only
        .address_space:  global
        .offset:         80
        .size:           8
        .value_kind:     global_buffer
      - .actual_access:  write_only
        .address_space:  global
        .offset:         88
        .size:           8
        .value_kind:     global_buffer
      - .actual_access:  read_only
        .address_space:  global
        .offset:         96
        .size:           8
        .value_kind:     global_buffer
      - .actual_access:  write_only
        .address_space:  global
        .offset:         104
        .size:           8
        .value_kind:     global_buffer
      - .actual_access:  read_only
        .address_space:  global
        .offset:         112
        .size:           8
        .value_kind:     global_buffer
      - .actual_access:  write_only
        .address_space:  global
        .offset:         120
        .size:           8
        .value_kind:     global_buffer
      - .actual_access:  write_only
        .address_space:  global
        .offset:         128
        .size:           8
        .value_kind:     global_buffer
      - .actual_access:  write_only
        .address_space:  global
        .offset:         136
        .size:           8
        .value_kind:     global_buffer
      - .actual_access:  write_only
        .address_space:  global
        .offset:         144
        .size:           8
        .value_kind:     global_buffer
    .group_segment_fixed_size: 4096
    .kernarg_segment_align: 8
    .kernarg_segment_size: 152
    .language:       OpenCL C
    .language_version:
      - 2
      - 0
    .max_flat_workgroup_size: 512
    .name:           _Z7k_frontPKfPmS0_S0_S0_S0_S0_S0_PDF16_S2_PfS3_S0_S2_S0_S2_S3_S3_S3_
    .private_segment_fixed_size: 0
    .sgpr_count:     88
    .sgpr_spill_count: 0
    .symbol:         _Z7k_frontPKfPmS0_S0_S0_S0_S0_S0_PDF16_S2_PfS3_S0_S2_S0_S2_S3_S3_S3_.kd
    .uniform_work_group_size: 1
    .uses_dynamic_stack: false
    .vgpr_count:     68
    .vgpr_spill_count: 0
    .wavefront_size: 64
  - .agpr_count:     256
    .args:
      - .actual_access:  read_only
        .address_space:  global
        .offset:         0
        .size:           8
        .value_kind:     global_buffer
      - .actual_access:  read_only
        .address_space:  global
        .offset:         8
        .size:           8
        .value_kind:     global_buffer
      - .actual_access:  read_only
        .address_space:  global
        .offset:         16
        .size:           8
        .value_kind:     global_buffer
      - .actual_access:  read_only
        .address_space:  global
        .offset:         24
        .size:           8
        .value_kind:     global_buffer
      - .actual_access:  read_only
        .address_space:  global
        .offset:         32
        .size:           8
        .value_kind:     global_buffer
      - .address_space:  global
        .offset:         40
        .size:           8
        .value_kind:     global_buffer
      - .actual_access:  write_only
        .address_space:  global
        .offset:         48
        .size:           8
        .value_kind:     global_buffer
      - .actual_access:  write_only
        .address_space:  global
        .offset:         56
        .size:           8
        .value_kind:     global_buffer
    .group_segment_fixed_size: 114688
    .kernarg_segment_align: 8
    .kernarg_segment_size: 64
    .language:       OpenCL C
    .language_version:
      - 2
      - 0
    .max_flat_workgroup_size: 256
    .name:           _Z6k_mainPKDF16_PKfS2_S2_PKmPjPfS6_
    .private_segment_fixed_size: 0
    .sgpr_count:     99
    .sgpr_spill_count: 0
    .symbol:         _Z6k_mainPKDF16_PKfS2_S2_PKmPjPfS6_.kd
    .uniform_work_group_size: 1
    .uses_dynamic_stack: false
    .vgpr_count:     488
    .vgpr_spill_count: 0
    .wavefront_size: 64
  - .agpr_count:     0
    .args:
      - .actual_access:  read_only
        .address_space:  global
        .offset:         0
        .size:           8
        .value_kind:     global_buffer
      - .actual_access:  read_only
        .address_space:  global
        .offset:         8
        .size:           8
        .value_kind:     global_buffer
      - .actual_access:  read_only
        .address_space:  global
        .offset:         16
        .size:           8
        .value_kind:     global_buffer
      - .actual_access:  read_only
        .address_space:  global
        .offset:         24
        .size:           8
        .value_kind:     global_buffer
      - .actual_access:  read_only
        .address_space:  global
        .offset:         32
        .size:           8
        .value_kind:     global_buffer
      - .actual_access:  read_only
        .address_space:  global
        .offset:         40
        .size:           8
        .value_kind:     global_buffer
      - .actual_access:  read_only
        .address_space:  global
        .offset:         48
        .size:           8
        .value_kind:     global_buffer
      - .actual_access:  read_only
        .address_space:  global
        .offset:         56
        .size:           8
        .value_kind:     global_buffer
      - .actual_access:  read_only
        .address_space:  global
        .offset:         64
        .size:           8
        .value_kind:     global_buffer
      - .actual_access:  write_only
        .address_space:  global
        .offset:         72
        .size:           8
        .value_kind:     global_buffer
      - .actual_access:  write_only
        .address_space:  global
        .offset:         80
        .size:           8
        .value_kind:     global_buffer
    .group_segment_fixed_size: 101632
    .kernarg_segment_align: 8
    .kernarg_segment_size: 88
    .language:       OpenCL C
    .language_version:
      - 2
      - 0
    .max_flat_workgroup_size: 256
    .name:           _Z7k_graphPKfS0_S0_S0_S0_S0_S0_S0_S0_PfS1_
    .private_segment_fixed_size: 0
    .sgpr_count:     25
    .sgpr_spill_count: 0
    .symbol:         _Z7k_graphPKfS0_S0_S0_S0_S0_S0_S0_S0_PfS1_.kd
    .uniform_work_group_size: 1
    .uses_dynamic_stack: false
    .vgpr_count:     118
    .vgpr_spill_count: 0
    .wavefront_size: 64
  - .agpr_count:     0
    .args:
      - .actual_access:  read_only
        .address_space:  global
        .offset:         0
        .size:           8
        .value_kind:     global_buffer
      - .actual_access:  read_only
        .address_space:  global
        .offset:         8
        .size:           8
        .value_kind:     global_buffer
      - .actual_access:  read_only
        .address_space:  global
        .offset:         16
        .size:           8
        .value_kind:     global_buffer
      - .actual_access:  read_only
        .address_space:  global
        .offset:         24
        .size:           8
        .value_kind:     global_buffer
      - .actual_access:  read_only
        .address_space:  global
        .offset:         32
        .size:           8
        .value_kind:     global_buffer
      - .actual_access:  read_only
        .address_space:  global
        .offset:         40
        .size:           8
        .value_kind:     global_buffer
      - .actual_access:  read_only
        .address_space:  global
        .offset:         48
        .size:           8
        .value_kind:     global_buffer
      - .address_space:  global
        .offset:         56
        .size:           8
        .value_kind:     global_buffer
      - .actual_access:  read_only
        .address_space:  global
        .offset:         64
        .size:           8
        .value_kind:     global_buffer
      - .actual_access:  read_only
        .address_space:  global
        .offset:         72
        .size:           8
        .value_kind:     global_buffer
      - .actual_access:  read_only
        .address_space:  global
        .offset:         80
        .size:           8
        .value_kind:     global_buffer
      - .address_space:  global
        .offset:         88
        .size:           8
        .value_kind:     global_buffer
      - .actual_access:  write_only
        .address_space:  global
        .offset:         96
        .size:           8
        .value_kind:     global_buffer
      - .actual_access:  write_only
        .address_space:  global
        .offset:         104
        .size:           8
        .value_kind:     global_buffer
      - .actual_access:  write_only
        .address_space:  global
        .offset:         112
        .size:           8
        .value_kind:     global_buffer
      - .actual_access:  read_only
        .address_space:  global
        .offset:         120
        .size:           8
        .value_kind:     global_buffer
      - .actual_access:  read_only
        .address_space:  global
        .offset:         128
        .size:           8
        .value_kind:     global_buffer
      - .actual_access:  read_only
        .address_space:  global
        .offset:         136
        .size:           8
        .value_kind:     global_buffer
      - .actual_access:  read_only
        .address_space:  global
        .offset:         144
        .size:           8
        .value_kind:     global_buffer
      - .actual_access:  read_only
        .address_space:  global
        .offset:         152
        .size:           8
        .value_kind:     global_buffer
      - .actual_access:  read_only
        .address_space:  global
        .offset:         160
        .size:           8
        .value_kind:     global_buffer
      - .actual_access:  read_only
        .address_space:  global
        .offset:         168
        .size:           8
        .value_kind:     global_buffer
    .group_segment_fixed_size: 53792
    .kernarg_segment_align: 8
    .kernarg_segment_size: 176
    .language:       OpenCL C
    .language_version:
      - 2
      - 0
    .max_flat_workgroup_size: 512
    .name:           _Z9k_redprepILi1EEvPKfPKjS1_S1_S1_S1_S1_PfPKDv8_DF16_S7_S1_PDF16_S4_S4_S4_PKiS7_S1_S1_S1_S4_S4_
    .private_segment_fixed_size: 0
    .sgpr_count:     106
    .sgpr_spill_count: 4
    .symbol:         _Z9k_redprepILi1EEvPKfPKjS1_S1_S1_S1_S1_PfPKDv8_DF16_S7_S1_PDF16_S4_S4_S4_PKiS7_S1_S1_S1_S4_S4_.kd
    .uniform_work_group_size: 1
    .uses_dynamic_stack: false
    .vgpr_count:     103
    .vgpr_spill_count: 0
    .wavefront_size: 64
  - .agpr_count:     0
    .args:
      - .actual_access:  read_only
        .address_space:  global
        .offset:         0
        .size:           8
        .value_kind:     global_buffer
      - .actual_access:  read_only
        .address_space:  global
        .offset:         8
        .size:           8
        .value_kind:     global_buffer
      - .actual_access:  read_only
        .address_space:  global
        .offset:         16
        .size:           8
        .value_kind:     global_buffer
      - .actual_access:  read_only
        .address_space:  global
        .offset:         24
        .size:           8
        .value_kind:     global_buffer
      - .actual_access:  read_only
        .address_space:  global
        .offset:         32
        .size:           8
        .value_kind:     global_buffer
      - .actual_access:  read_only
        .address_space:  global
        .offset:         40
        .size:           8
        .value_kind:     global_buffer
      - .actual_access:  read_only
        .address_space:  global
        .offset:         48
        .size:           8
        .value_kind:     global_buffer
      - .address_space:  global
        .offset:         56
        .size:           8
        .value_kind:     global_buffer
      - .actual_access:  read_only
        .address_space:  global
        .offset:         64
        .size:           8
        .value_kind:     global_buffer
      - .actual_access:  read_only
        .address_space:  global
        .offset:         72
        .size:           8
        .value_kind:     global_buffer
      - .actual_access:  read_only
        .address_space:  global
        .offset:         80
        .size:           8
        .value_kind:     global_buffer
      - .actual_access:  read_only
        .address_space:  global
        .offset:         88
        .size:           8
        .value_kind:     global_buffer
      - .actual_access:  read_only
        .address_space:  global
        .offset:         96
        .size:           8
        .value_kind:     global_buffer
      - .actual_access:  read_only
        .address_space:  global
        .offset:         104
        .size:           8
        .value_kind:     global_buffer
      - .actual_access:  read_only
        .address_space:  global
        .offset:         112
        .size:           8
        .value_kind:     global_buffer
      - .actual_access:  read_only
        .address_space:  global
        .offset:         120
        .size:           8
        .value_kind:     global_buffer
      - .actual_access:  read_only
        .address_space:  global
        .offset:         128
        .size:           8
        .value_kind:     global_buffer
      - .actual_access:  read_only
        .address_space:  global
        .offset:         136
        .size:           8
        .value_kind:     global_buffer
      - .actual_access:  read_only
        .address_space:  global
        .offset:         144
        .size:           8
        .value_kind:     global_buffer
      - .actual_access:  read_only
        .address_space:  global
        .offset:         152
        .size:           8
        .value_kind:     global_buffer
      - .actual_access:  write_only
        .address_space:  global
        .offset:         160
        .size:           8
        .value_kind:     global_buffer
      - .address_space:  global
        .offset:         168
        .size:           8
        .value_kind:     global_buffer
    .group_segment_fixed_size: 66688
    .kernarg_segment_align: 8
    .kernarg_segment_size: 176
    .language:       OpenCL C
    .language_version:
      - 2
      - 0
    .max_flat_workgroup_size: 512
    .name:           _Z9k_redprepILi2EEvPKfPKjS1_S1_S1_S1_S1_PfPKDv8_DF16_S7_S1_PDF16_S4_S4_S4_PKiS7_S1_S1_S1_S4_S4_
    .private_segment_fixed_size: 0
    .sgpr_count:     102
    .sgpr_spill_count: 0
    .symbol:         _Z9k_redprepILi2EEvPKfPKjS1_S1_S1_S1_S1_PfPKDv8_DF16_S7_S1_PDF16_S4_S4_S4_PKiS7_S1_S1_S1_S4_S4_.kd
    .uniform_work_group_size: 1
    .uses_dynamic_stack: false
    .vgpr_count:     106
    .vgpr_spill_count: 0
    .wavefront_size: 64
